# router tails: xor-32 transposing exchange done with v_permlane32_swap in registers instead of select + ds_bpermute (both rows)
# baseline (speedup 1.0000x reference)
; #define LAS __attribute__((address_space(3)))
; __device__ __forceinline__ void phase_norm2(const Params& p, const Ctx& F, const int l) {
;     ...
;         f32x2 lg[16];
;         unsigned wro = (unsigned)(uintptr_t)wr; asm volatile("" : "+v"(wro));
;         const LAS float* wr2 = (const LAS float*)(uintptr_t)wro;
; #pragma unroll
;         for (int e = 0; e < 16; ++e) { f32x2 a = {0.f, 0.f};
; #pragma unroll
;             for (int j = 0; j < 8; ++j) { const f32x4 w = *((const LAS f32x4*)(wr2 + e * DM) + F.lane + 64 * j);
; #pragma unroll
;                 for (int c = 0; c < 4; ++c) a += vv[j][c] * w[c]; }
;             lg[e] = a; }
.LBB0_937:
	s_or_b64 exec, exec, s[12:13]
	v_mov_b32_e32 v1, v35
	s_nop 0
	v_lshl_add_u32 v182, v132, 4, v1
	v_add_u32_e32 v244, 0x10000, v182
	ds_read_b128 v[224:227], v182
	ds_read_b128 v[228:231], v182 offset:1024
	ds_read_b128 v[232:235], v182 offset:2048
	ds_read_b128 v[236:239], v182 offset:3072
	s_waitcnt lgkmcnt(3)
	v_pk_fma_f32 v[156:157], v[124:125], v[224:225], 0 op_sel_hi:[1,0,0]
	s_nop 0
	v_pk_fma_f32 v[152:153], v[126:127], v[224:225], v[156:157] op_sel:[0,1,0]
	s_nop 0
	v_pk_fma_f32 v[152:153], v[128:129], v[226:227], v[152:153] op_sel_hi:[1,0,1]
	v_mov_b32_e32 v154, v227
	v_pk_fma_f32 v[156:157], v[130:131], v[154:155], v[152:153] op_sel_hi:[1,0,1]
	ds_read_b128 v[240:243], v182 offset:4096
	s_waitcnt lgkmcnt(3)
	v_pk_fma_f32 v[156:157], v[112:113], v[228:229], v[156:157] op_sel_hi:[1,0,1]
	s_nop 0
	v_pk_fma_f32 v[152:153], v[114:115], v[228:229], v[156:157] op_sel:[0,1,0]
	s_nop 0
	v_pk_fma_f32 v[152:153], v[118:119], v[230:231], v[152:153] op_sel_hi:[1,0,1]
	v_mov_b32_e32 v154, v231
	v_pk_fma_f32 v[156:157], v[122:123], v[154:155], v[152:153] op_sel_hi:[1,0,1]
	ds_read_b128 v[224:227], v182 offset:5120
	s_waitcnt lgkmcnt(3)
	v_pk_fma_f32 v[156:157], v[108:109], v[232:233], v[156:157] op_sel_hi:[1,0,1]
	s_nop 0
	v_pk_fma_f32 v[152:153], v[110:111], v[232:233], v[156:157] op_sel:[0,1,0]
	s_nop 0
	v_pk_fma_f32 v[152:153], v[116:117], v[234:235], v[152:153] op_sel_hi:[1,0,1]
	v_mov_b32_e32 v154, v235
	v_pk_fma_f32 v[156:157], v[120:121], v[154:155], v[152:153] op_sel_hi:[1,0,1]
	ds_read_b128 v[228:231], v182 offset:6144
	s_waitcnt lgkmcnt(3)
	v_pk_fma_f32 v[156:157], v[96:97], v[236:237], v[156:157] op_sel_hi:[1,0,1]
	s_nop 0
	v_pk_fma_f32 v[152:153], v[98:99], v[236:237], v[156:157] op_sel:[0,1,0]
	s_nop 0
	v_pk_fma_f32 v[152:153], v[102:103], v[238:239], v[152:153] op_sel_hi:[1,0,1]
	v_mov_b32_e32 v154, v239
	v_pk_fma_f32 v[156:157], v[106:107], v[154:155], v[152:153] op_sel_hi:[1,0,1]
	ds_read_b128 v[232:235], v182 offset:7168
	s_waitcnt lgkmcnt(3)
	v_pk_fma_f32 v[156:157], v[92:93], v[240:241], v[156:157] op_sel_hi:[1,0,1]
	s_nop 0
	v_pk_fma_f32 v[152:153], v[94:95], v[240:241], v[156:157] op_sel:[0,1,0]
	s_nop 0
	v_pk_fma_f32 v[152:153], v[100:101], v[242:243], v[152:153] op_sel_hi:[1,0,1]
	v_mov_b32_e32 v154, v243
	v_pk_fma_f32 v[156:157], v[104:105], v[154:155], v[152:153] op_sel_hi:[1,0,1]
	ds_read_b128 v[236:239], v182 offset:8192
	s_waitcnt lgkmcnt(3)
	v_pk_fma_f32 v[156:157], v[80:81], v[224:225], v[156:157] op_sel_hi:[1,0,1]
	s_nop 0
	v_pk_fma_f32 v[152:153], v[82:83], v[224:225], v[156:157] op_sel:[0,1,0]
	s_nop 0
	v_pk_fma_f32 v[152:153], v[86:87], v[226:227], v[152:153] op_sel_hi:[1,0,1]
	v_mov_b32_e32 v154, v227
	v_pk_fma_f32 v[156:157], v[90:91], v[154:155], v[152:153] op_sel_hi:[1,0,1]
	ds_read_b128 v[240:243], v182 offset:9216
	s_waitcnt lgkmcnt(3)
	v_pk_fma_f32 v[156:157], v[76:77], v[228:229], v[156:157] op_sel_hi:[1,0,1]
	s_nop 0
	v_pk_fma_f32 v[152:153], v[78:79], v[228:229], v[156:157] op_sel:[0,1,0]
	s_nop 0
	v_pk_fma_f32 v[152:153], v[84:85], v[230:231], v[152:153] op_sel_hi:[1,0,1]
	v_mov_b32_e32 v154, v231
	v_pk_fma_f32 v[156:157], v[88:89], v[154:155], v[152:153] op_sel_hi:[1,0,1]
	ds_read_b128 v[224:227], v182 offset:10240
	s_waitcnt lgkmcnt(3)
	v_pk_fma_f32 v[156:157], v[68:69], v[232:233], v[156:157] op_sel_hi:[1,0,1]
	s_nop 0
	v_pk_fma_f32 v[152:153], v[70:71], v[232:233], v[156:157] op_sel:[0,1,0]
	s_nop 0
	v_pk_fma_f32 v[152:153], v[72:73], v[234:235], v[152:153] op_sel_hi:[1,0,1]
	v_mov_b32_e32 v154, v235
	v_pk_fma_f32 v[152:153], v[74:75], v[154:155], v[152:153] op_sel_hi:[1,0,1]
	ds_read_b128 v[228:231], v182 offset:11264
	s_waitcnt lgkmcnt(3)
	v_pk_fma_f32 v[158:159], v[124:125], v[236:237], 0 op_sel_hi:[1,0,0]
	s_nop 0
	v_pk_fma_f32 v[154:155], v[126:127], v[236:237], v[158:159] op_sel:[0,1,0]
	s_nop 0
	v_pk_fma_f32 v[154:155], v[128:129], v[238:239], v[154:155] op_sel_hi:[1,0,1]
	v_mov_b32_e32 v156, v239
	v_pk_fma_f32 v[158:159], v[130:131], v[156:157], v[154:155] op_sel_hi:[1,0,1]
	ds_read_b128 v[232:235], v182 offset:12288
	s_waitcnt lgkmcnt(3)
	v_pk_fma_f32 v[158:159], v[112:113], v[240:241], v[158:159] op_sel_hi:[1,0,1]
	s_nop 0
	v_pk_fma_f32 v[154:155], v[114:115], v[240:241], v[158:159] op_sel:[0,1,0]
	s_nop 0
	v_pk_fma_f32 v[154:155], v[118:119], v[242:243], v[154:155] op_sel_hi:[1,0,1]
	v_mov_b32_e32 v156, v243
	v_pk_fma_f32 v[158:159], v[122:123], v[156:157], v[154:155] op_sel_hi:[1,0,1]
	ds_read_b128 v[236:239], v182 offset:13312
	s_waitcnt lgkmcnt(3)
	v_pk_fma_f32 v[158:159], v[108:109], v[224:225], v[158:159] op_sel_hi:[1,0,1]
	s_nop 0
	v_pk_fma_f32 v[154:155], v[110:111], v[224:225], v[158:159] op_sel:[0,1,0]
	s_nop 0
	v_pk_fma_f32 v[154:155], v[116:117], v[226:227], v[154:155] op_sel_hi:[1,0,1]
	v_mov_b32_e32 v156, v227
	v_pk_fma_f32 v[158:159], v[120:121], v[156:157], v[154:155] op_sel_hi:[1,0,1]
	ds_read_b128 v[240:243], v182 offset:14336
	s_waitcnt lgkmcnt(3)
	v_pk_fma_f32 v[158:159], v[96:97], v[228:229], v[158:159] op_sel_hi:[1,0,1]
	s_nop 0
	v_pk_fma_f32 v[154:155], v[98:99], v[228:229], v[158:159] op_sel:[0,1,0]
	s_nop 0
	v_pk_fma_f32 v[154:155], v[102:103], v[230:231], v[154:155] op_sel_hi:[1,0,1]
	v_mov_b32_e32 v156, v231
	v_pk_fma_f32 v[158:159], v[106:107], v[156:157], v[154:155] op_sel_hi:[1,0,1]
	ds_read_b128 v[224:227], v182 offset:15360
	s_waitcnt lgkmcnt(3)
	v_pk_fma_f32 v[158:159], v[92:93], v[232:233], v[158:159] op_sel_hi:[1,0,1]
	s_nop 0
	v_pk_fma_f32 v[154:155], v[94:95], v[232:233], v[158:159] op_sel:[0,1,0]
	s_nop 0
	v_pk_fma_f32 v[154:155], v[100:101], v[234:235], v[154:155] op_sel_hi:[1,0,1]
	v_mov_b32_e32 v156, v235
	v_pk_fma_f32 v[158:159], v[104:105], v[156:157], v[154:155] op_sel_hi:[1,0,1]
	ds_read_b128 v[228:231], v182 offset:16384
	s_waitcnt lgkmcnt(3)
; #define LAS __attribute__((address_space(3)))
; __device__ __forceinline__ void phase_norm2(const Params& p, const Ctx& F, const int l) {
;     ...
; #pragma unroll
;         for (int e = 0; e < 16; ++e) { f32x2 a = {0.f, 0.f};
; #pragma unroll
;             for (int j = 0; j < 8; ++j) { const f32x4 w = *((const LAS f32x4*)(wr2 + e * DM) + F.lane + 64 * j);
; #pragma unroll
;                 for (int c = 0; c < 4; ++c) a += vv[j][c] * w[c]; }
;             lg[e] = a; }
	v_pk_fma_f32 v[158:159], v[80:81], v[236:237], v[158:159] op_sel_hi:[1,0,1]
	s_nop 0
	v_pk_fma_f32 v[154:155], v[82:83], v[236:237], v[158:159] op_sel:[0,1,0]
	s_nop 0
	v_pk_fma_f32 v[154:155], v[86:87], v[238:239], v[154:155] op_sel_hi:[1,0,1]
	v_mov_b32_e32 v156, v239
	v_pk_fma_f32 v[158:159], v[90:91], v[156:157], v[154:155] op_sel_hi:[1,0,1]
	ds_read_b128 v[232:235], v182 offset:17408
	s_waitcnt lgkmcnt(3)
	v_pk_fma_f32 v[158:159], v[76:77], v[240:241], v[158:159] op_sel_hi:[1,0,1]
	s_nop 0
	v_pk_fma_f32 v[154:155], v[78:79], v[240:241], v[158:159] op_sel:[0,1,0]
	s_nop 0
	v_pk_fma_f32 v[154:155], v[84:85], v[242:243], v[154:155] op_sel_hi:[1,0,1]
	v_mov_b32_e32 v156, v243
	v_pk_fma_f32 v[158:159], v[88:89], v[156:157], v[154:155] op_sel_hi:[1,0,1]
	ds_read_b128 v[236:239], v182 offset:18432
	s_waitcnt lgkmcnt(3)
	v_pk_fma_f32 v[158:159], v[68:69], v[224:225], v[158:159] op_sel_hi:[1,0,1]
	s_nop 0
	v_pk_fma_f32 v[154:155], v[70:71], v[224:225], v[158:159] op_sel:[0,1,0]
	s_nop 0
	v_pk_fma_f32 v[154:155], v[72:73], v[226:227], v[154:155] op_sel_hi:[1,0,1]
	v_mov_b32_e32 v156, v227
	v_pk_fma_f32 v[154:155], v[74:75], v[156:157], v[154:155] op_sel_hi:[1,0,1]
	ds_read_b128 v[240:243], v182 offset:19456
	s_waitcnt lgkmcnt(3)
	v_pk_fma_f32 v[160:161], v[124:125], v[228:229], 0 op_sel_hi:[1,0,0]
	s_nop 0
	v_pk_fma_f32 v[156:157], v[126:127], v[228:229], v[160:161] op_sel:[0,1,0]
	s_nop 0
	v_pk_fma_f32 v[156:157], v[128:129], v[230:231], v[156:157] op_sel_hi:[1,0,1]
	v_mov_b32_e32 v158, v231
	v_pk_fma_f32 v[160:161], v[130:131], v[158:159], v[156:157] op_sel_hi:[1,0,1]
	ds_read_b128 v[224:227], v182 offset:20480
	s_waitcnt lgkmcnt(3)
	v_pk_fma_f32 v[160:161], v[112:113], v[232:233], v[160:161] op_sel_hi:[1,0,1]
	s_nop 0
	v_pk_fma_f32 v[156:157], v[114:115], v[232:233], v[160:161] op_sel:[0,1,0]
	s_nop 0
	v_pk_fma_f32 v[156:157], v[118:119], v[234:235], v[156:157] op_sel_hi:[1,0,1]
	v_mov_b32_e32 v158, v235
	v_pk_fma_f32 v[160:161], v[122:123], v[158:159], v[156:157] op_sel_hi:[1,0,1]
	ds_read_b128 v[228:231], v182 offset:21504
	s_waitcnt lgkmcnt(3)
	v_pk_fma_f32 v[160:161], v[108:109], v[236:237], v[160:161] op_sel_hi:[1,0,1]
	s_nop 0
	v_pk_fma_f32 v[156:157], v[110:111], v[236:237], v[160:161] op_sel:[0,1,0]
	s_nop 0
	v_pk_fma_f32 v[156:157], v[116:117], v[238:239], v[156:157] op_sel_hi:[1,0,1]
	v_mov_b32_e32 v158, v239
	v_pk_fma_f32 v[160:161], v[120:121], v[158:159], v[156:157] op_sel_hi:[1,0,1]
	ds_read_b128 v[232:235], v182 offset:22528
	s_waitcnt lgkmcnt(3)
	v_pk_fma_f32 v[160:161], v[96:97], v[240:241], v[160:161] op_sel_hi:[1,0,1]
	s_nop 0
	v_pk_fma_f32 v[156:157], v[98:99], v[240:241], v[160:161] op_sel:[0,1,0]
	s_nop 0
	v_pk_fma_f32 v[156:157], v[102:103], v[242:243], v[156:157] op_sel_hi:[1,0,1]
	v_mov_b32_e32 v158, v243
	v_pk_fma_f32 v[160:161], v[106:107], v[158:159], v[156:157] op_sel_hi:[1,0,1]
	ds_read_b128 v[236:239], v182 offset:23552
	s_waitcnt lgkmcnt(3)
	v_pk_fma_f32 v[160:161], v[92:93], v[224:225], v[160:161] op_sel_hi:[1,0,1]
	s_nop 0
	v_pk_fma_f32 v[156:157], v[94:95], v[224:225], v[160:161] op_sel:[0,1,0]
	s_nop 0
	v_pk_fma_f32 v[156:157], v[100:101], v[226:227], v[156:157] op_sel_hi:[1,0,1]
	v_mov_b32_e32 v158, v227
	v_pk_fma_f32 v[160:161], v[104:105], v[158:159], v[156:157] op_sel_hi:[1,0,1]
	ds_read_b128 v[240:243], v182 offset:24576
	s_waitcnt lgkmcnt(3)
	v_pk_fma_f32 v[160:161], v[80:81], v[228:229], v[160:161] op_sel_hi:[1,0,1]
	s_nop 0
	v_pk_fma_f32 v[156:157], v[82:83], v[228:229], v[160:161] op_sel:[0,1,0]
	s_nop 0
	v_pk_fma_f32 v[156:157], v[86:87], v[230:231], v[156:157] op_sel_hi:[1,0,1]
	v_mov_b32_e32 v158, v231
	v_pk_fma_f32 v[160:161], v[90:91], v[158:159], v[156:157] op_sel_hi:[1,0,1]
	ds_read_b128 v[224:227], v182 offset:25600
	s_waitcnt lgkmcnt(3)
	v_pk_fma_f32 v[160:161], v[76:77], v[232:233], v[160:161] op_sel_hi:[1,0,1]
	s_nop 0
	v_pk_fma_f32 v[156:157], v[78:79], v[232:233], v[160:161] op_sel:[0,1,0]
	s_nop 0
	v_pk_fma_f32 v[156:157], v[84:85], v[234:235], v[156:157] op_sel_hi:[1,0,1]
	v_mov_b32_e32 v158, v235
	v_pk_fma_f32 v[160:161], v[88:89], v[158:159], v[156:157] op_sel_hi:[1,0,1]
	ds_read_b128 v[228:231], v182 offset:26624
	s_waitcnt lgkmcnt(3)
	v_pk_fma_f32 v[160:161], v[68:69], v[236:237], v[160:161] op_sel_hi:[1,0,1]
	s_nop 0
	v_pk_fma_f32 v[156:157], v[70:71], v[236:237], v[160:161] op_sel:[0,1,0]
	s_nop 0
	v_pk_fma_f32 v[156:157], v[72:73], v[238:239], v[156:157] op_sel_hi:[1,0,1]
	v_mov_b32_e32 v158, v239
	v_pk_fma_f32 v[156:157], v[74:75], v[158:159], v[156:157] op_sel_hi:[1,0,1]
	ds_read_b128 v[232:235], v182 offset:27648
	s_waitcnt lgkmcnt(3)
	v_pk_fma_f32 v[162:163], v[124:125], v[240:241], 0 op_sel_hi:[1,0,0]
	s_nop 0
	v_pk_fma_f32 v[158:159], v[126:127], v[240:241], v[162:163] op_sel:[0,1,0]
	s_nop 0
	v_pk_fma_f32 v[158:159], v[128:129], v[242:243], v[158:159] op_sel_hi:[1,0,1]
	v_mov_b32_e32 v160, v243
	v_pk_fma_f32 v[162:163], v[130:131], v[160:161], v[158:159] op_sel_hi:[1,0,1]
	ds_read_b128 v[236:239], v182 offset:28672
	s_waitcnt lgkmcnt(3)
	v_pk_fma_f32 v[162:163], v[112:113], v[224:225], v[162:163] op_sel_hi:[1,0,1]
	s_nop 0
	v_pk_fma_f32 v[158:159], v[114:115], v[224:225], v[162:163] op_sel:[0,1,0]
	s_nop 0
	v_pk_fma_f32 v[158:159], v[118:119], v[226:227], v[158:159] op_sel_hi:[1,0,1]
	v_mov_b32_e32 v160, v227
	v_pk_fma_f32 v[162:163], v[122:123], v[160:161], v[158:159] op_sel_hi:[1,0,1]
	ds_read_b128 v[240:243], v182 offset:29696
	s_waitcnt lgkmcnt(3)
	v_pk_fma_f32 v[162:163], v[108:109], v[228:229], v[162:163] op_sel_hi:[1,0,1]
	s_nop 0
	v_pk_fma_f32 v[158:159], v[110:111], v[228:229], v[162:163] op_sel:[0,1,0]
	s_nop 0
	v_pk_fma_f32 v[158:159], v[116:117], v[230:231], v[158:159] op_sel_hi:[1,0,1]
	v_mov_b32_e32 v160, v231
	v_pk_fma_f32 v[162:163], v[120:121], v[160:161], v[158:159] op_sel_hi:[1,0,1]
	ds_read_b128 v[224:227], v182 offset:30720
	s_waitcnt lgkmcnt(3)
; #define LAS __attribute__((address_space(3)))
; __device__ __forceinline__ void phase_norm2(const Params& p, const Ctx& F, const int l) {
;     ...
;         f32x2 lg[16];
;         unsigned wro = (unsigned)(uintptr_t)wr; asm volatile("" : "+v"(wro));
;         const LAS float* wr2 = (const LAS float*)(uintptr_t)wro;
; #pragma unroll
;         for (int e = 0; e < 16; ++e) { f32x2 a = {0.f, 0.f};
; #pragma unroll
;             for (int j = 0; j < 8; ++j) { const f32x4 w = *((const LAS f32x4*)(wr2 + e * DM) + F.lane + 64 * j);
; #pragma unroll
;                 for (int c = 0; c < 4; ++c) a += vv[j][c] * w[c]; }
;             lg[e] = a; }
	v_pk_fma_f32 v[162:163], v[96:97], v[232:233], v[162:163] op_sel_hi:[1,0,1]
	s_nop 0
	v_pk_fma_f32 v[158:159], v[98:99], v[232:233], v[162:163] op_sel:[0,1,0]
	s_nop 0
	v_pk_fma_f32 v[158:159], v[102:103], v[234:235], v[158:159] op_sel_hi:[1,0,1]
	v_mov_b32_e32 v160, v235
	v_pk_fma_f32 v[162:163], v[106:107], v[160:161], v[158:159] op_sel_hi:[1,0,1]
	ds_read_b128 v[228:231], v182 offset:31744
	s_waitcnt lgkmcnt(3)
	v_pk_fma_f32 v[162:163], v[92:93], v[236:237], v[162:163] op_sel_hi:[1,0,1]
	s_nop 0
	v_pk_fma_f32 v[158:159], v[94:95], v[236:237], v[162:163] op_sel:[0,1,0]
	s_nop 0
	v_pk_fma_f32 v[158:159], v[100:101], v[238:239], v[158:159] op_sel_hi:[1,0,1]
	v_mov_b32_e32 v160, v239
	v_pk_fma_f32 v[162:163], v[104:105], v[160:161], v[158:159] op_sel_hi:[1,0,1]
	ds_read_b128 v[232:235], v182 offset:32768
	s_waitcnt lgkmcnt(3)
	v_pk_fma_f32 v[162:163], v[80:81], v[240:241], v[162:163] op_sel_hi:[1,0,1]
	s_nop 0
	v_pk_fma_f32 v[158:159], v[82:83], v[240:241], v[162:163] op_sel:[0,1,0]
	s_nop 0
	v_pk_fma_f32 v[158:159], v[86:87], v[242:243], v[158:159] op_sel_hi:[1,0,1]
	v_mov_b32_e32 v160, v243
	v_pk_fma_f32 v[162:163], v[90:91], v[160:161], v[158:159] op_sel_hi:[1,0,1]
	ds_read_b128 v[236:239], v182 offset:33792
	s_waitcnt lgkmcnt(3)
	v_pk_fma_f32 v[162:163], v[76:77], v[224:225], v[162:163] op_sel_hi:[1,0,1]
	s_nop 0
	v_pk_fma_f32 v[158:159], v[78:79], v[224:225], v[162:163] op_sel:[0,1,0]
	s_nop 0
	v_pk_fma_f32 v[158:159], v[84:85], v[226:227], v[158:159] op_sel_hi:[1,0,1]
	v_mov_b32_e32 v160, v227
	v_pk_fma_f32 v[162:163], v[88:89], v[160:161], v[158:159] op_sel_hi:[1,0,1]
	ds_read_b128 v[240:243], v182 offset:34816
	s_waitcnt lgkmcnt(3)
	v_pk_fma_f32 v[162:163], v[68:69], v[228:229], v[162:163] op_sel_hi:[1,0,1]
	s_nop 0
	v_pk_fma_f32 v[158:159], v[70:71], v[228:229], v[162:163] op_sel:[0,1,0]
	s_nop 0
	v_pk_fma_f32 v[158:159], v[72:73], v[230:231], v[158:159] op_sel_hi:[1,0,1]
	v_mov_b32_e32 v160, v231
	v_pk_fma_f32 v[158:159], v[74:75], v[160:161], v[158:159] op_sel_hi:[1,0,1]
	ds_read_b128 v[224:227], v182 offset:35840
	s_waitcnt lgkmcnt(3)
	v_pk_fma_f32 v[164:165], v[124:125], v[232:233], 0 op_sel_hi:[1,0,0]
	s_nop 0
	v_pk_fma_f32 v[160:161], v[126:127], v[232:233], v[164:165] op_sel:[0,1,0]
	s_nop 0
	v_pk_fma_f32 v[160:161], v[128:129], v[234:235], v[160:161] op_sel_hi:[1,0,1]
	v_mov_b32_e32 v162, v235
	v_pk_fma_f32 v[164:165], v[130:131], v[162:163], v[160:161] op_sel_hi:[1,0,1]
	ds_read_b128 v[228:231], v182 offset:36864
	s_waitcnt lgkmcnt(3)
	v_pk_fma_f32 v[164:165], v[112:113], v[236:237], v[164:165] op_sel_hi:[1,0,1]
	s_nop 0
	v_pk_fma_f32 v[160:161], v[114:115], v[236:237], v[164:165] op_sel:[0,1,0]
	s_nop 0
	v_pk_fma_f32 v[160:161], v[118:119], v[238:239], v[160:161] op_sel_hi:[1,0,1]
	v_mov_b32_e32 v162, v239
	v_pk_fma_f32 v[164:165], v[122:123], v[162:163], v[160:161] op_sel_hi:[1,0,1]
	ds_read_b128 v[232:235], v182 offset:37888
	s_waitcnt lgkmcnt(3)
	v_pk_fma_f32 v[164:165], v[108:109], v[240:241], v[164:165] op_sel_hi:[1,0,1]
	s_nop 0
	v_pk_fma_f32 v[160:161], v[110:111], v[240:241], v[164:165] op_sel:[0,1,0]
	s_nop 0
	v_pk_fma_f32 v[160:161], v[116:117], v[242:243], v[160:161] op_sel_hi:[1,0,1]
	v_mov_b32_e32 v162, v243
	v_pk_fma_f32 v[164:165], v[120:121], v[162:163], v[160:161] op_sel_hi:[1,0,1]
	ds_read_b128 v[236:239], v182 offset:38912
	s_waitcnt lgkmcnt(3)
	v_pk_fma_f32 v[164:165], v[96:97], v[224:225], v[164:165] op_sel_hi:[1,0,1]
	s_nop 0
	v_pk_fma_f32 v[160:161], v[98:99], v[224:225], v[164:165] op_sel:[0,1,0]
	s_nop 0
	v_pk_fma_f32 v[160:161], v[102:103], v[226:227], v[160:161] op_sel_hi:[1,0,1]
	v_mov_b32_e32 v162, v227
	v_pk_fma_f32 v[164:165], v[106:107], v[162:163], v[160:161] op_sel_hi:[1,0,1]
	ds_read_b128 v[240:243], v182 offset:39936
	s_waitcnt lgkmcnt(3)
	v_pk_fma_f32 v[164:165], v[92:93], v[228:229], v[164:165] op_sel_hi:[1,0,1]
	s_nop 0
	v_pk_fma_f32 v[160:161], v[94:95], v[228:229], v[164:165] op_sel:[0,1,0]
	s_nop 0
	v_pk_fma_f32 v[160:161], v[100:101], v[230:231], v[160:161] op_sel_hi:[1,0,1]
	v_mov_b32_e32 v162, v231
	v_pk_fma_f32 v[164:165], v[104:105], v[162:163], v[160:161] op_sel_hi:[1,0,1]
	ds_read_b128 v[224:227], v182 offset:40960
	s_waitcnt lgkmcnt(3)
	v_pk_fma_f32 v[164:165], v[80:81], v[232:233], v[164:165] op_sel_hi:[1,0,1]
	s_nop 0
	v_pk_fma_f32 v[160:161], v[82:83], v[232:233], v[164:165] op_sel:[0,1,0]
	s_nop 0
	v_pk_fma_f32 v[160:161], v[86:87], v[234:235], v[160:161] op_sel_hi:[1,0,1]
	v_mov_b32_e32 v162, v235
	v_pk_fma_f32 v[164:165], v[90:91], v[162:163], v[160:161] op_sel_hi:[1,0,1]
	ds_read_b128 v[228:231], v182 offset:41984
	s_waitcnt lgkmcnt(3)
	v_pk_fma_f32 v[164:165], v[76:77], v[236:237], v[164:165] op_sel_hi:[1,0,1]
	s_nop 0
	v_pk_fma_f32 v[160:161], v[78:79], v[236:237], v[164:165] op_sel:[0,1,0]
	s_nop 0
	v_pk_fma_f32 v[160:161], v[84:85], v[238:239], v[160:161] op_sel_hi:[1,0,1]
	v_mov_b32_e32 v162, v239
	v_pk_fma_f32 v[164:165], v[88:89], v[162:163], v[160:161] op_sel_hi:[1,0,1]
	ds_read_b128 v[232:235], v182 offset:43008
	s_waitcnt lgkmcnt(3)
	v_pk_fma_f32 v[164:165], v[68:69], v[240:241], v[164:165] op_sel_hi:[1,0,1]
	s_nop 0
	v_pk_fma_f32 v[160:161], v[70:71], v[240:241], v[164:165] op_sel:[0,1,0]
	s_nop 0
	v_pk_fma_f32 v[160:161], v[72:73], v[242:243], v[160:161] op_sel_hi:[1,0,1]
	v_mov_b32_e32 v162, v243
	v_pk_fma_f32 v[160:161], v[74:75], v[162:163], v[160:161] op_sel_hi:[1,0,1]
	ds_read_b128 v[236:239], v182 offset:44032
	s_waitcnt lgkmcnt(3)
	v_pk_fma_f32 v[166:167], v[124:125], v[224:225], 0 op_sel_hi:[1,0,0]
	s_nop 0
	v_pk_fma_f32 v[162:163], v[126:127], v[224:225], v[166:167] op_sel:[0,1,0]
	s_nop 0
	v_pk_fma_f32 v[162:163], v[128:129], v[226:227], v[162:163] op_sel_hi:[1,0,1]
	v_mov_b32_e32 v164, v227
	v_pk_fma_f32 v[166:167], v[130:131], v[164:165], v[162:163] op_sel_hi:[1,0,1]
	ds_read_b128 v[240:243], v182 offset:45056
	s_waitcnt lgkmcnt(3)
; #define LAS __attribute__((address_space(3)))
; __device__ __forceinline__ void phase_norm2(const Params& p, const Ctx& F, const int l) {
;     ...
;         f32x2 lg[16];
;         unsigned wro = (unsigned)(uintptr_t)wr; asm volatile("" : "+v"(wro));
;         const LAS float* wr2 = (const LAS float*)(uintptr_t)wro;
; #pragma unroll
;         for (int e = 0; e < 16; ++e) { f32x2 a = {0.f, 0.f};
; #pragma unroll
;             for (int j = 0; j < 8; ++j) { const f32x4 w = *((const LAS f32x4*)(wr2 + e * DM) + F.lane + 64 * j);
; #pragma unroll
;                 for (int c = 0; c < 4; ++c) a += vv[j][c] * w[c]; }
;             lg[e] = a; }
	v_pk_fma_f32 v[166:167], v[112:113], v[228:229], v[166:167] op_sel_hi:[1,0,1]
	s_nop 0
	v_pk_fma_f32 v[162:163], v[114:115], v[228:229], v[166:167] op_sel:[0,1,0]
	s_nop 0
	v_pk_fma_f32 v[162:163], v[118:119], v[230:231], v[162:163] op_sel_hi:[1,0,1]
	v_mov_b32_e32 v164, v231
	v_pk_fma_f32 v[166:167], v[122:123], v[164:165], v[162:163] op_sel_hi:[1,0,1]
	ds_read_b128 v[224:227], v182 offset:46080
	s_waitcnt lgkmcnt(3)
	v_pk_fma_f32 v[166:167], v[108:109], v[232:233], v[166:167] op_sel_hi:[1,0,1]
	s_nop 0
	v_pk_fma_f32 v[162:163], v[110:111], v[232:233], v[166:167] op_sel:[0,1,0]
	s_nop 0
	v_pk_fma_f32 v[162:163], v[116:117], v[234:235], v[162:163] op_sel_hi:[1,0,1]
	v_mov_b32_e32 v164, v235
	v_pk_fma_f32 v[166:167], v[120:121], v[164:165], v[162:163] op_sel_hi:[1,0,1]
	ds_read_b128 v[228:231], v182 offset:47104
	s_waitcnt lgkmcnt(3)
	v_pk_fma_f32 v[166:167], v[96:97], v[236:237], v[166:167] op_sel_hi:[1,0,1]
	s_nop 0
	v_pk_fma_f32 v[162:163], v[98:99], v[236:237], v[166:167] op_sel:[0,1,0]
	s_nop 0
	v_pk_fma_f32 v[162:163], v[102:103], v[238:239], v[162:163] op_sel_hi:[1,0,1]
	v_mov_b32_e32 v164, v239
	v_pk_fma_f32 v[166:167], v[106:107], v[164:165], v[162:163] op_sel_hi:[1,0,1]
	ds_read_b128 v[232:235], v182 offset:48128
	s_waitcnt lgkmcnt(3)
	v_pk_fma_f32 v[166:167], v[92:93], v[240:241], v[166:167] op_sel_hi:[1,0,1]
	s_nop 0
	v_pk_fma_f32 v[162:163], v[94:95], v[240:241], v[166:167] op_sel:[0,1,0]
	s_nop 0
	v_pk_fma_f32 v[162:163], v[100:101], v[242:243], v[162:163] op_sel_hi:[1,0,1]
	v_mov_b32_e32 v164, v243
	v_pk_fma_f32 v[166:167], v[104:105], v[164:165], v[162:163] op_sel_hi:[1,0,1]
	ds_read_b128 v[236:239], v182 offset:49152
	s_waitcnt lgkmcnt(3)
	v_pk_fma_f32 v[166:167], v[80:81], v[224:225], v[166:167] op_sel_hi:[1,0,1]
	s_nop 0
	v_pk_fma_f32 v[162:163], v[82:83], v[224:225], v[166:167] op_sel:[0,1,0]
	s_nop 0
	v_pk_fma_f32 v[162:163], v[86:87], v[226:227], v[162:163] op_sel_hi:[1,0,1]
	v_mov_b32_e32 v164, v227
	v_pk_fma_f32 v[166:167], v[90:91], v[164:165], v[162:163] op_sel_hi:[1,0,1]
	ds_read_b128 v[240:243], v182 offset:50176
	s_waitcnt lgkmcnt(3)
	v_pk_fma_f32 v[166:167], v[76:77], v[228:229], v[166:167] op_sel_hi:[1,0,1]
	s_nop 0
	v_pk_fma_f32 v[162:163], v[78:79], v[228:229], v[166:167] op_sel:[0,1,0]
	s_nop 0
	v_pk_fma_f32 v[162:163], v[84:85], v[230:231], v[162:163] op_sel_hi:[1,0,1]
	v_mov_b32_e32 v164, v231
	v_pk_fma_f32 v[166:167], v[88:89], v[164:165], v[162:163] op_sel_hi:[1,0,1]
	ds_read_b128 v[224:227], v182 offset:51200
	s_waitcnt lgkmcnt(3)
	v_pk_fma_f32 v[166:167], v[68:69], v[232:233], v[166:167] op_sel_hi:[1,0,1]
	s_nop 0
	v_pk_fma_f32 v[162:163], v[70:71], v[232:233], v[166:167] op_sel:[0,1,0]
	s_nop 0
	v_pk_fma_f32 v[162:163], v[72:73], v[234:235], v[162:163] op_sel_hi:[1,0,1]
	v_mov_b32_e32 v164, v235
	v_pk_fma_f32 v[162:163], v[74:75], v[164:165], v[162:163] op_sel_hi:[1,0,1]
	ds_read_b128 v[228:231], v182 offset:52224
	s_waitcnt lgkmcnt(3)
	v_pk_fma_f32 v[168:169], v[124:125], v[236:237], 0 op_sel_hi:[1,0,0]
	s_nop 0
	v_pk_fma_f32 v[164:165], v[126:127], v[236:237], v[168:169] op_sel:[0,1,0]
	s_nop 0
	v_pk_fma_f32 v[164:165], v[128:129], v[238:239], v[164:165] op_sel_hi:[1,0,1]
	v_mov_b32_e32 v166, v239
	v_pk_fma_f32 v[168:169], v[130:131], v[166:167], v[164:165] op_sel_hi:[1,0,1]
	ds_read_b128 v[232:235], v182 offset:53248
	s_waitcnt lgkmcnt(3)
	v_pk_fma_f32 v[168:169], v[112:113], v[240:241], v[168:169] op_sel_hi:[1,0,1]
	s_nop 0
	v_pk_fma_f32 v[164:165], v[114:115], v[240:241], v[168:169] op_sel:[0,1,0]
	s_nop 0
	v_pk_fma_f32 v[164:165], v[118:119], v[242:243], v[164:165] op_sel_hi:[1,0,1]
	v_mov_b32_e32 v166, v243
	v_pk_fma_f32 v[168:169], v[122:123], v[166:167], v[164:165] op_sel_hi:[1,0,1]
	ds_read_b128 v[236:239], v182 offset:54272
	s_waitcnt lgkmcnt(3)
	v_pk_fma_f32 v[168:169], v[108:109], v[224:225], v[168:169] op_sel_hi:[1,0,1]
	s_nop 0
	v_pk_fma_f32 v[164:165], v[110:111], v[224:225], v[168:169] op_sel:[0,1,0]
	s_nop 0
	v_pk_fma_f32 v[164:165], v[116:117], v[226:227], v[164:165] op_sel_hi:[1,0,1]
	v_mov_b32_e32 v166, v227
	v_pk_fma_f32 v[168:169], v[120:121], v[166:167], v[164:165] op_sel_hi:[1,0,1]
	ds_read_b128 v[240:243], v182 offset:55296
	s_waitcnt lgkmcnt(3)
	v_pk_fma_f32 v[168:169], v[96:97], v[228:229], v[168:169] op_sel_hi:[1,0,1]
	s_nop 0
	v_pk_fma_f32 v[164:165], v[98:99], v[228:229], v[168:169] op_sel:[0,1,0]
	s_nop 0
	v_pk_fma_f32 v[164:165], v[102:103], v[230:231], v[164:165] op_sel_hi:[1,0,1]
	v_mov_b32_e32 v166, v231
	v_pk_fma_f32 v[168:169], v[106:107], v[166:167], v[164:165] op_sel_hi:[1,0,1]
	ds_read_b128 v[224:227], v182 offset:56320
	s_waitcnt lgkmcnt(3)
	v_pk_fma_f32 v[168:169], v[92:93], v[232:233], v[168:169] op_sel_hi:[1,0,1]
	s_nop 0
	v_pk_fma_f32 v[164:165], v[94:95], v[232:233], v[168:169] op_sel:[0,1,0]
	s_nop 0
	v_pk_fma_f32 v[164:165], v[100:101], v[234:235], v[164:165] op_sel_hi:[1,0,1]
	v_mov_b32_e32 v166, v235
	v_pk_fma_f32 v[168:169], v[104:105], v[166:167], v[164:165] op_sel_hi:[1,0,1]
	ds_read_b128 v[228:231], v182 offset:57344
	s_waitcnt lgkmcnt(3)
	v_pk_fma_f32 v[168:169], v[80:81], v[236:237], v[168:169] op_sel_hi:[1,0,1]
	s_nop 0
	v_pk_fma_f32 v[164:165], v[82:83], v[236:237], v[168:169] op_sel:[0,1,0]
	s_nop 0
	v_pk_fma_f32 v[164:165], v[86:87], v[238:239], v[164:165] op_sel_hi:[1,0,1]
	v_mov_b32_e32 v166, v239
	v_pk_fma_f32 v[168:169], v[90:91], v[166:167], v[164:165] op_sel_hi:[1,0,1]
	ds_read_b128 v[232:235], v182 offset:58368
	s_waitcnt lgkmcnt(3)
; #define LAS __attribute__((address_space(3)))
; __device__ __forceinline__ void phase_norm2(const Params& p, const Ctx& F, const int l) {
;     ...
;         f32x2 lg[16];
;         unsigned wro = (unsigned)(uintptr_t)wr; asm volatile("" : "+v"(wro));
;         const LAS float* wr2 = (const LAS float*)(uintptr_t)wro;
; #pragma unroll
;         for (int e = 0; e < 16; ++e) { f32x2 a = {0.f, 0.f};
; #pragma unroll
;             for (int j = 0; j < 8; ++j) { const f32x4 w = *((const LAS f32x4*)(wr2 + e * DM) + F.lane + 64 * j);
; #pragma unroll
;                 for (int c = 0; c < 4; ++c) a += vv[j][c] * w[c]; }
;             lg[e] = a; }
	v_pk_fma_f32 v[168:169], v[76:77], v[240:241], v[168:169] op_sel_hi:[1,0,1]
	s_nop 0
	v_pk_fma_f32 v[164:165], v[78:79], v[240:241], v[168:169] op_sel:[0,1,0]
	s_nop 0
	v_pk_fma_f32 v[164:165], v[84:85], v[242:243], v[164:165] op_sel_hi:[1,0,1]
	v_mov_b32_e32 v166, v243
	v_pk_fma_f32 v[168:169], v[88:89], v[166:167], v[164:165] op_sel_hi:[1,0,1]
	ds_read_b128 v[236:239], v182 offset:59392
	s_waitcnt lgkmcnt(3)
	v_pk_fma_f32 v[168:169], v[68:69], v[224:225], v[168:169] op_sel_hi:[1,0,1]
	s_nop 0
	v_pk_fma_f32 v[164:165], v[70:71], v[224:225], v[168:169] op_sel:[0,1,0]
	s_nop 0
	v_pk_fma_f32 v[164:165], v[72:73], v[226:227], v[164:165] op_sel_hi:[1,0,1]
	v_mov_b32_e32 v166, v227
	v_pk_fma_f32 v[164:165], v[74:75], v[166:167], v[164:165] op_sel_hi:[1,0,1]
	ds_read_b128 v[240:243], v182 offset:60416
	s_waitcnt lgkmcnt(3)
	v_pk_fma_f32 v[170:171], v[124:125], v[228:229], 0 op_sel_hi:[1,0,0]
	s_nop 0
	v_pk_fma_f32 v[166:167], v[126:127], v[228:229], v[170:171] op_sel:[0,1,0]
	s_nop 0
	v_pk_fma_f32 v[166:167], v[128:129], v[230:231], v[166:167] op_sel_hi:[1,0,1]
	v_mov_b32_e32 v168, v231
	v_pk_fma_f32 v[170:171], v[130:131], v[168:169], v[166:167] op_sel_hi:[1,0,1]
	ds_read_b128 v[224:227], v182 offset:61440
	s_waitcnt lgkmcnt(3)
	v_pk_fma_f32 v[170:171], v[112:113], v[232:233], v[170:171] op_sel_hi:[1,0,1]
	s_nop 0
	v_pk_fma_f32 v[166:167], v[114:115], v[232:233], v[170:171] op_sel:[0,1,0]
	s_nop 0
	v_pk_fma_f32 v[166:167], v[118:119], v[234:235], v[166:167] op_sel_hi:[1,0,1]
	v_mov_b32_e32 v168, v235
	v_pk_fma_f32 v[170:171], v[122:123], v[168:169], v[166:167] op_sel_hi:[1,0,1]
	ds_read_b128 v[228:231], v182 offset:62464
	s_waitcnt lgkmcnt(3)
	v_pk_fma_f32 v[170:171], v[108:109], v[236:237], v[170:171] op_sel_hi:[1,0,1]
	s_nop 0
	v_pk_fma_f32 v[166:167], v[110:111], v[236:237], v[170:171] op_sel:[0,1,0]
	s_nop 0
	v_pk_fma_f32 v[166:167], v[116:117], v[238:239], v[166:167] op_sel_hi:[1,0,1]
	v_mov_b32_e32 v168, v239
	v_pk_fma_f32 v[170:171], v[120:121], v[168:169], v[166:167] op_sel_hi:[1,0,1]
	ds_read_b128 v[232:235], v182 offset:63488
	s_waitcnt lgkmcnt(3)
	v_pk_fma_f32 v[170:171], v[96:97], v[240:241], v[170:171] op_sel_hi:[1,0,1]
	s_nop 0
	v_pk_fma_f32 v[166:167], v[98:99], v[240:241], v[170:171] op_sel:[0,1,0]
	s_nop 0
	v_pk_fma_f32 v[166:167], v[102:103], v[242:243], v[166:167] op_sel_hi:[1,0,1]
	v_mov_b32_e32 v168, v243
	v_pk_fma_f32 v[170:171], v[106:107], v[168:169], v[166:167] op_sel_hi:[1,0,1]
	ds_read_b128 v[236:239], v182 offset:64512
	s_waitcnt lgkmcnt(3)
	v_pk_fma_f32 v[170:171], v[92:93], v[224:225], v[170:171] op_sel_hi:[1,0,1]
	s_nop 0
	v_pk_fma_f32 v[166:167], v[94:95], v[224:225], v[170:171] op_sel:[0,1,0]
	s_nop 0
	v_pk_fma_f32 v[166:167], v[100:101], v[226:227], v[166:167] op_sel_hi:[1,0,1]
	v_mov_b32_e32 v168, v227
	v_pk_fma_f32 v[170:171], v[104:105], v[168:169], v[166:167] op_sel_hi:[1,0,1]
	ds_read_b128 v[240:243], v244
	s_waitcnt lgkmcnt(3)
	v_pk_fma_f32 v[170:171], v[80:81], v[228:229], v[170:171] op_sel_hi:[1,0,1]
	s_nop 0
	v_pk_fma_f32 v[166:167], v[82:83], v[228:229], v[170:171] op_sel:[0,1,0]
	s_nop 0
	v_pk_fma_f32 v[166:167], v[86:87], v[230:231], v[166:167] op_sel_hi:[1,0,1]
	v_mov_b32_e32 v168, v231
	v_pk_fma_f32 v[170:171], v[90:91], v[168:169], v[166:167] op_sel_hi:[1,0,1]
	ds_read_b128 v[224:227], v244 offset:1024
	s_waitcnt lgkmcnt(3)
	v_pk_fma_f32 v[170:171], v[76:77], v[232:233], v[170:171] op_sel_hi:[1,0,1]
	s_nop 0
	v_pk_fma_f32 v[166:167], v[78:79], v[232:233], v[170:171] op_sel:[0,1,0]
	s_nop 0
	v_pk_fma_f32 v[166:167], v[84:85], v[234:235], v[166:167] op_sel_hi:[1,0,1]
	v_mov_b32_e32 v168, v235
	v_pk_fma_f32 v[170:171], v[88:89], v[168:169], v[166:167] op_sel_hi:[1,0,1]
	ds_read_b128 v[228:231], v244 offset:2048
	s_waitcnt lgkmcnt(3)
	v_pk_fma_f32 v[170:171], v[68:69], v[236:237], v[170:171] op_sel_hi:[1,0,1]
	s_nop 0
	v_pk_fma_f32 v[166:167], v[70:71], v[236:237], v[170:171] op_sel:[0,1,0]
	s_nop 0
	v_pk_fma_f32 v[166:167], v[72:73], v[238:239], v[166:167] op_sel_hi:[1,0,1]
	v_mov_b32_e32 v168, v239
	v_pk_fma_f32 v[166:167], v[74:75], v[168:169], v[166:167] op_sel_hi:[1,0,1]
	ds_read_b128 v[232:235], v244 offset:3072
	s_waitcnt lgkmcnt(3)
	v_pk_fma_f32 v[172:173], v[124:125], v[240:241], 0 op_sel_hi:[1,0,0]
	s_nop 0
	v_pk_fma_f32 v[168:169], v[126:127], v[240:241], v[172:173] op_sel:[0,1,0]
	s_nop 0
	v_pk_fma_f32 v[168:169], v[128:129], v[242:243], v[168:169] op_sel_hi:[1,0,1]
	v_mov_b32_e32 v170, v243
	v_pk_fma_f32 v[172:173], v[130:131], v[170:171], v[168:169] op_sel_hi:[1,0,1]
	ds_read_b128 v[236:239], v244 offset:4096
	s_waitcnt lgkmcnt(3)
	v_pk_fma_f32 v[172:173], v[112:113], v[224:225], v[172:173] op_sel_hi:[1,0,1]
	s_nop 0
	v_pk_fma_f32 v[168:169], v[114:115], v[224:225], v[172:173] op_sel:[0,1,0]
	s_nop 0
	v_pk_fma_f32 v[168:169], v[118:119], v[226:227], v[168:169] op_sel_hi:[1,0,1]
	v_mov_b32_e32 v170, v227
	v_pk_fma_f32 v[172:173], v[122:123], v[170:171], v[168:169] op_sel_hi:[1,0,1]
	ds_read_b128 v[240:243], v244 offset:5120
	s_waitcnt lgkmcnt(3)
	v_pk_fma_f32 v[172:173], v[108:109], v[228:229], v[172:173] op_sel_hi:[1,0,1]
	s_nop 0
	v_pk_fma_f32 v[168:169], v[110:111], v[228:229], v[172:173] op_sel:[0,1,0]
	s_nop 0
	v_pk_fma_f32 v[168:169], v[116:117], v[230:231], v[168:169] op_sel_hi:[1,0,1]
	v_mov_b32_e32 v170, v231
	v_pk_fma_f32 v[172:173], v[120:121], v[170:171], v[168:169] op_sel_hi:[1,0,1]
	ds_read_b128 v[224:227], v244 offset:6144
	s_waitcnt lgkmcnt(3)
	v_pk_fma_f32 v[172:173], v[96:97], v[232:233], v[172:173] op_sel_hi:[1,0,1]
	s_nop 0
	v_pk_fma_f32 v[168:169], v[98:99], v[232:233], v[172:173] op_sel:[0,1,0]
	s_nop 0
	v_pk_fma_f32 v[168:169], v[102:103], v[234:235], v[168:169] op_sel_hi:[1,0,1]
	v_mov_b32_e32 v170, v235
	v_pk_fma_f32 v[172:173], v[106:107], v[170:171], v[168:169] op_sel_hi:[1,0,1]
	ds_read_b128 v[228:231], v244 offset:7168
	s_waitcnt lgkmcnt(3)
; #define LAS __attribute__((address_space(3)))
; __device__ __forceinline__ void phase_norm2(const Params& p, const Ctx& F, const int l) {
;     ...
;         f32x2 lg[16];
;         unsigned wro = (unsigned)(uintptr_t)wr; asm volatile("" : "+v"(wro));
;         const LAS float* wr2 = (const LAS float*)(uintptr_t)wro;
; #pragma unroll
;         for (int e = 0; e < 16; ++e) { f32x2 a = {0.f, 0.f};
; #pragma unroll
;             for (int j = 0; j < 8; ++j) { const f32x4 w = *((const LAS f32x4*)(wr2 + e * DM) + F.lane + 64 * j);
; #pragma unroll
;                 for (int c = 0; c < 4; ++c) a += vv[j][c] * w[c]; }
;             lg[e] = a; }
	v_pk_fma_f32 v[172:173], v[92:93], v[236:237], v[172:173] op_sel_hi:[1,0,1]
	s_nop 0
	v_pk_fma_f32 v[168:169], v[94:95], v[236:237], v[172:173] op_sel:[0,1,0]
	s_nop 0
	v_pk_fma_f32 v[168:169], v[100:101], v[238:239], v[168:169] op_sel_hi:[1,0,1]
	v_mov_b32_e32 v170, v239
	v_pk_fma_f32 v[172:173], v[104:105], v[170:171], v[168:169] op_sel_hi:[1,0,1]
	ds_read_b128 v[232:235], v244 offset:8192
	s_waitcnt lgkmcnt(3)
	v_pk_fma_f32 v[172:173], v[80:81], v[240:241], v[172:173] op_sel_hi:[1,0,1]
	s_nop 0
	v_pk_fma_f32 v[168:169], v[82:83], v[240:241], v[172:173] op_sel:[0,1,0]
	s_nop 0
	v_pk_fma_f32 v[168:169], v[86:87], v[242:243], v[168:169] op_sel_hi:[1,0,1]
	v_mov_b32_e32 v170, v243
	v_pk_fma_f32 v[172:173], v[90:91], v[170:171], v[168:169] op_sel_hi:[1,0,1]
	ds_read_b128 v[236:239], v244 offset:9216
	s_waitcnt lgkmcnt(3)
	v_pk_fma_f32 v[172:173], v[76:77], v[224:225], v[172:173] op_sel_hi:[1,0,1]
	s_nop 0
	v_pk_fma_f32 v[168:169], v[78:79], v[224:225], v[172:173] op_sel:[0,1,0]
	s_nop 0
	v_pk_fma_f32 v[168:169], v[84:85], v[226:227], v[168:169] op_sel_hi:[1,0,1]
	v_mov_b32_e32 v170, v227
	v_pk_fma_f32 v[172:173], v[88:89], v[170:171], v[168:169] op_sel_hi:[1,0,1]
	ds_read_b128 v[240:243], v244 offset:10240
	s_waitcnt lgkmcnt(3)
	v_pk_fma_f32 v[172:173], v[68:69], v[228:229], v[172:173] op_sel_hi:[1,0,1]
	s_nop 0
	v_pk_fma_f32 v[168:169], v[70:71], v[228:229], v[172:173] op_sel:[0,1,0]
	s_nop 0
	v_pk_fma_f32 v[168:169], v[72:73], v[230:231], v[168:169] op_sel_hi:[1,0,1]
	v_mov_b32_e32 v170, v231
	v_pk_fma_f32 v[168:169], v[74:75], v[170:171], v[168:169] op_sel_hi:[1,0,1]
	ds_read_b128 v[224:227], v244 offset:11264
	s_waitcnt lgkmcnt(3)
	v_pk_fma_f32 v[174:175], v[124:125], v[232:233], 0 op_sel_hi:[1,0,0]
	s_nop 0
	v_pk_fma_f32 v[170:171], v[126:127], v[232:233], v[174:175] op_sel:[0,1,0]
	s_nop 0
	v_pk_fma_f32 v[170:171], v[128:129], v[234:235], v[170:171] op_sel_hi:[1,0,1]
	v_mov_b32_e32 v172, v235
	v_pk_fma_f32 v[174:175], v[130:131], v[172:173], v[170:171] op_sel_hi:[1,0,1]
	ds_read_b128 v[228:231], v244 offset:12288
	s_waitcnt lgkmcnt(3)
	v_pk_fma_f32 v[174:175], v[112:113], v[236:237], v[174:175] op_sel_hi:[1,0,1]
	s_nop 0
	v_pk_fma_f32 v[170:171], v[114:115], v[236:237], v[174:175] op_sel:[0,1,0]
	s_nop 0
	v_pk_fma_f32 v[170:171], v[118:119], v[238:239], v[170:171] op_sel_hi:[1,0,1]
	v_mov_b32_e32 v172, v239
	v_pk_fma_f32 v[174:175], v[122:123], v[172:173], v[170:171] op_sel_hi:[1,0,1]
	ds_read_b128 v[232:235], v244 offset:13312
	s_waitcnt lgkmcnt(3)
	v_pk_fma_f32 v[174:175], v[108:109], v[240:241], v[174:175] op_sel_hi:[1,0,1]
	s_nop 0
	v_pk_fma_f32 v[170:171], v[110:111], v[240:241], v[174:175] op_sel:[0,1,0]
	s_nop 0
	v_pk_fma_f32 v[170:171], v[116:117], v[242:243], v[170:171] op_sel_hi:[1,0,1]
	v_mov_b32_e32 v172, v243
	v_pk_fma_f32 v[174:175], v[120:121], v[172:173], v[170:171] op_sel_hi:[1,0,1]
	ds_read_b128 v[236:239], v244 offset:14336
	s_waitcnt lgkmcnt(3)
	v_pk_fma_f32 v[174:175], v[96:97], v[224:225], v[174:175] op_sel_hi:[1,0,1]
	s_nop 0
	v_pk_fma_f32 v[170:171], v[98:99], v[224:225], v[174:175] op_sel:[0,1,0]
	s_nop 0
	v_pk_fma_f32 v[170:171], v[102:103], v[226:227], v[170:171] op_sel_hi:[1,0,1]
	v_mov_b32_e32 v172, v227
	v_pk_fma_f32 v[174:175], v[106:107], v[172:173], v[170:171] op_sel_hi:[1,0,1]
	ds_read_b128 v[240:243], v244 offset:15360
	s_waitcnt lgkmcnt(3)
	v_pk_fma_f32 v[174:175], v[92:93], v[228:229], v[174:175] op_sel_hi:[1,0,1]
	s_nop 0
	v_pk_fma_f32 v[170:171], v[94:95], v[228:229], v[174:175] op_sel:[0,1,0]
	s_nop 0
	v_pk_fma_f32 v[170:171], v[100:101], v[230:231], v[170:171] op_sel_hi:[1,0,1]
	v_mov_b32_e32 v172, v231
	v_pk_fma_f32 v[174:175], v[104:105], v[172:173], v[170:171] op_sel_hi:[1,0,1]
	ds_read_b128 v[224:227], v244 offset:16384
	s_waitcnt lgkmcnt(3)
	v_pk_fma_f32 v[174:175], v[80:81], v[232:233], v[174:175] op_sel_hi:[1,0,1]
	s_nop 0
	v_pk_fma_f32 v[170:171], v[82:83], v[232:233], v[174:175] op_sel:[0,1,0]
	s_nop 0
	v_pk_fma_f32 v[170:171], v[86:87], v[234:235], v[170:171] op_sel_hi:[1,0,1]
	v_mov_b32_e32 v172, v235
	v_pk_fma_f32 v[174:175], v[90:91], v[172:173], v[170:171] op_sel_hi:[1,0,1]
	ds_read_b128 v[228:231], v244 offset:17408
	s_waitcnt lgkmcnt(3)
	v_pk_fma_f32 v[174:175], v[76:77], v[236:237], v[174:175] op_sel_hi:[1,0,1]
	s_nop 0
	v_pk_fma_f32 v[170:171], v[78:79], v[236:237], v[174:175] op_sel:[0,1,0]
	s_nop 0
	v_pk_fma_f32 v[170:171], v[84:85], v[238:239], v[170:171] op_sel_hi:[1,0,1]
	v_mov_b32_e32 v172, v239
	v_pk_fma_f32 v[174:175], v[88:89], v[172:173], v[170:171] op_sel_hi:[1,0,1]
	ds_read_b128 v[232:235], v244 offset:18432
	s_waitcnt lgkmcnt(3)
	v_pk_fma_f32 v[174:175], v[68:69], v[240:241], v[174:175] op_sel_hi:[1,0,1]
	s_nop 0
	v_pk_fma_f32 v[170:171], v[70:71], v[240:241], v[174:175] op_sel:[0,1,0]
	s_nop 0
	v_pk_fma_f32 v[170:171], v[72:73], v[242:243], v[170:171] op_sel_hi:[1,0,1]
	v_mov_b32_e32 v172, v243
	v_pk_fma_f32 v[170:171], v[74:75], v[172:173], v[170:171] op_sel_hi:[1,0,1]
	ds_read_b128 v[236:239], v244 offset:19456
	s_waitcnt lgkmcnt(3)
	v_pk_fma_f32 v[176:177], v[124:125], v[224:225], 0 op_sel_hi:[1,0,0]
	s_nop 0
	v_pk_fma_f32 v[172:173], v[126:127], v[224:225], v[176:177] op_sel:[0,1,0]
	s_nop 0
	v_pk_fma_f32 v[172:173], v[128:129], v[226:227], v[172:173] op_sel_hi:[1,0,1]
	v_mov_b32_e32 v174, v227
	v_pk_fma_f32 v[176:177], v[130:131], v[174:175], v[172:173] op_sel_hi:[1,0,1]
	ds_read_b128 v[240:243], v244 offset:20480
	s_waitcnt lgkmcnt(3)
	v_pk_fma_f32 v[176:177], v[112:113], v[228:229], v[176:177] op_sel_hi:[1,0,1]
	s_nop 0
	v_pk_fma_f32 v[172:173], v[114:115], v[228:229], v[176:177] op_sel:[0,1,0]
	s_nop 0
	v_pk_fma_f32 v[172:173], v[118:119], v[230:231], v[172:173] op_sel_hi:[1,0,1]
	v_mov_b32_e32 v174, v231
	v_pk_fma_f32 v[176:177], v[122:123], v[174:175], v[172:173] op_sel_hi:[1,0,1]
	ds_read_b128 v[224:227], v244 offset:21504
	s_waitcnt lgkmcnt(3)
; #define LAS __attribute__((address_space(3)))
; __device__ __forceinline__ void phase_norm2(const Params& p, const Ctx& F, const int l) {
;     ...
;         f32x2 lg[16];
;         unsigned wro = (unsigned)(uintptr_t)wr; asm volatile("" : "+v"(wro));
;         const LAS float* wr2 = (const LAS float*)(uintptr_t)wro;
; #pragma unroll
;         for (int e = 0; e < 16; ++e) { f32x2 a = {0.f, 0.f};
; #pragma unroll
;             for (int j = 0; j < 8; ++j) { const f32x4 w = *((const LAS f32x4*)(wr2 + e * DM) + F.lane + 64 * j);
; #pragma unroll
;                 for (int c = 0; c < 4; ++c) a += vv[j][c] * w[c]; }
;             lg[e] = a; }
	v_pk_fma_f32 v[176:177], v[108:109], v[232:233], v[176:177] op_sel_hi:[1,0,1]
	s_nop 0
	v_pk_fma_f32 v[172:173], v[110:111], v[232:233], v[176:177] op_sel:[0,1,0]
	s_nop 0
	v_pk_fma_f32 v[172:173], v[116:117], v[234:235], v[172:173] op_sel_hi:[1,0,1]
	v_mov_b32_e32 v174, v235
	v_pk_fma_f32 v[176:177], v[120:121], v[174:175], v[172:173] op_sel_hi:[1,0,1]
	ds_read_b128 v[228:231], v244 offset:22528
	s_waitcnt lgkmcnt(3)
	v_pk_fma_f32 v[176:177], v[96:97], v[236:237], v[176:177] op_sel_hi:[1,0,1]
	s_nop 0
	v_pk_fma_f32 v[172:173], v[98:99], v[236:237], v[176:177] op_sel:[0,1,0]
	s_nop 0
	v_pk_fma_f32 v[172:173], v[102:103], v[238:239], v[172:173] op_sel_hi:[1,0,1]
	v_mov_b32_e32 v174, v239
	v_pk_fma_f32 v[176:177], v[106:107], v[174:175], v[172:173] op_sel_hi:[1,0,1]
	ds_read_b128 v[232:235], v244 offset:23552
	s_waitcnt lgkmcnt(3)
	v_pk_fma_f32 v[176:177], v[92:93], v[240:241], v[176:177] op_sel_hi:[1,0,1]
	s_nop 0
	v_pk_fma_f32 v[172:173], v[94:95], v[240:241], v[176:177] op_sel:[0,1,0]
	s_nop 0
	v_pk_fma_f32 v[172:173], v[100:101], v[242:243], v[172:173] op_sel_hi:[1,0,1]
	v_mov_b32_e32 v174, v243
	v_pk_fma_f32 v[176:177], v[104:105], v[174:175], v[172:173] op_sel_hi:[1,0,1]
	ds_read_b128 v[236:239], v244 offset:24576
	s_waitcnt lgkmcnt(3)
	v_pk_fma_f32 v[176:177], v[80:81], v[224:225], v[176:177] op_sel_hi:[1,0,1]
	s_nop 0
	v_pk_fma_f32 v[172:173], v[82:83], v[224:225], v[176:177] op_sel:[0,1,0]
	s_nop 0
	v_pk_fma_f32 v[172:173], v[86:87], v[226:227], v[172:173] op_sel_hi:[1,0,1]
	v_mov_b32_e32 v174, v227
	v_pk_fma_f32 v[176:177], v[90:91], v[174:175], v[172:173] op_sel_hi:[1,0,1]
	ds_read_b128 v[240:243], v244 offset:25600
	s_waitcnt lgkmcnt(3)
	v_pk_fma_f32 v[176:177], v[76:77], v[228:229], v[176:177] op_sel_hi:[1,0,1]
	s_nop 0
	v_pk_fma_f32 v[172:173], v[78:79], v[228:229], v[176:177] op_sel:[0,1,0]
	s_nop 0
	v_pk_fma_f32 v[172:173], v[84:85], v[230:231], v[172:173] op_sel_hi:[1,0,1]
	v_mov_b32_e32 v174, v231
	v_pk_fma_f32 v[176:177], v[88:89], v[174:175], v[172:173] op_sel_hi:[1,0,1]
	ds_read_b128 v[224:227], v244 offset:26624
	s_waitcnt lgkmcnt(3)
	v_pk_fma_f32 v[176:177], v[68:69], v[232:233], v[176:177] op_sel_hi:[1,0,1]
	s_nop 0
	v_pk_fma_f32 v[172:173], v[70:71], v[232:233], v[176:177] op_sel:[0,1,0]
	s_nop 0
	v_pk_fma_f32 v[172:173], v[72:73], v[234:235], v[172:173] op_sel_hi:[1,0,1]
	v_mov_b32_e32 v174, v235
	v_pk_fma_f32 v[172:173], v[74:75], v[174:175], v[172:173] op_sel_hi:[1,0,1]
	ds_read_b128 v[228:231], v244 offset:27648
	s_waitcnt lgkmcnt(3)
	v_pk_fma_f32 v[178:179], v[124:125], v[236:237], 0 op_sel_hi:[1,0,0]
	s_nop 0
	v_pk_fma_f32 v[174:175], v[126:127], v[236:237], v[178:179] op_sel:[0,1,0]
	s_nop 0
	v_pk_fma_f32 v[174:175], v[128:129], v[238:239], v[174:175] op_sel_hi:[1,0,1]
	v_mov_b32_e32 v176, v239
	v_pk_fma_f32 v[178:179], v[130:131], v[176:177], v[174:175] op_sel_hi:[1,0,1]
	ds_read_b128 v[232:235], v244 offset:28672
	s_waitcnt lgkmcnt(3)
	v_pk_fma_f32 v[178:179], v[112:113], v[240:241], v[178:179] op_sel_hi:[1,0,1]
	s_nop 0
	v_pk_fma_f32 v[174:175], v[114:115], v[240:241], v[178:179] op_sel:[0,1,0]
	s_nop 0
	v_pk_fma_f32 v[174:175], v[118:119], v[242:243], v[174:175] op_sel_hi:[1,0,1]
	v_mov_b32_e32 v176, v243
	v_pk_fma_f32 v[178:179], v[122:123], v[176:177], v[174:175] op_sel_hi:[1,0,1]
	ds_read_b128 v[236:239], v244 offset:29696
	s_waitcnt lgkmcnt(3)
	v_pk_fma_f32 v[178:179], v[108:109], v[224:225], v[178:179] op_sel_hi:[1,0,1]
	s_nop 0
	v_pk_fma_f32 v[174:175], v[110:111], v[224:225], v[178:179] op_sel:[0,1,0]
	s_nop 0
	v_pk_fma_f32 v[174:175], v[116:117], v[226:227], v[174:175] op_sel_hi:[1,0,1]
	v_mov_b32_e32 v176, v227
	v_pk_fma_f32 v[178:179], v[120:121], v[176:177], v[174:175] op_sel_hi:[1,0,1]
	ds_read_b128 v[240:243], v244 offset:30720
	s_waitcnt lgkmcnt(3)
	v_pk_fma_f32 v[178:179], v[96:97], v[228:229], v[178:179] op_sel_hi:[1,0,1]
	s_nop 0
	v_pk_fma_f32 v[174:175], v[98:99], v[228:229], v[178:179] op_sel:[0,1,0]
	s_nop 0
	v_pk_fma_f32 v[174:175], v[102:103], v[230:231], v[174:175] op_sel_hi:[1,0,1]
	v_mov_b32_e32 v176, v231
	v_pk_fma_f32 v[178:179], v[106:107], v[176:177], v[174:175] op_sel_hi:[1,0,1]
	ds_read_b128 v[224:227], v244 offset:31744
	s_waitcnt lgkmcnt(3)
	v_pk_fma_f32 v[178:179], v[92:93], v[232:233], v[178:179] op_sel_hi:[1,0,1]
	s_nop 0
	v_pk_fma_f32 v[174:175], v[94:95], v[232:233], v[178:179] op_sel:[0,1,0]
	s_nop 0
	v_pk_fma_f32 v[174:175], v[100:101], v[234:235], v[174:175] op_sel_hi:[1,0,1]
	v_mov_b32_e32 v176, v235
	v_pk_fma_f32 v[178:179], v[104:105], v[176:177], v[174:175] op_sel_hi:[1,0,1]
	ds_read_b128 v[228:231], v244 offset:32768
	s_waitcnt lgkmcnt(3)
	v_pk_fma_f32 v[178:179], v[80:81], v[236:237], v[178:179] op_sel_hi:[1,0,1]
	s_nop 0
	v_pk_fma_f32 v[174:175], v[82:83], v[236:237], v[178:179] op_sel:[0,1,0]
	s_nop 0
	v_pk_fma_f32 v[174:175], v[86:87], v[238:239], v[174:175] op_sel_hi:[1,0,1]
	v_mov_b32_e32 v176, v239
	v_pk_fma_f32 v[178:179], v[90:91], v[176:177], v[174:175] op_sel_hi:[1,0,1]
	ds_read_b128 v[232:235], v244 offset:33792
	s_waitcnt lgkmcnt(3)
	v_pk_fma_f32 v[178:179], v[76:77], v[240:241], v[178:179] op_sel_hi:[1,0,1]
	s_nop 0
	v_pk_fma_f32 v[174:175], v[78:79], v[240:241], v[178:179] op_sel:[0,1,0]
	s_nop 0
	v_pk_fma_f32 v[174:175], v[84:85], v[242:243], v[174:175] op_sel_hi:[1,0,1]
	v_mov_b32_e32 v176, v243
	v_pk_fma_f32 v[178:179], v[88:89], v[176:177], v[174:175] op_sel_hi:[1,0,1]
	ds_read_b128 v[236:239], v244 offset:34816
	s_waitcnt lgkmcnt(3)
; #define LAS __attribute__((address_space(3)))
; __device__ __forceinline__ void phase_norm2(const Params& p, const Ctx& F, const int l) {
;     ...
;         f32x2 lg[16];
;         unsigned wro = (unsigned)(uintptr_t)wr; asm volatile("" : "+v"(wro));
;         const LAS float* wr2 = (const LAS float*)(uintptr_t)wro;
; #pragma unroll
;         for (int e = 0; e < 16; ++e) { f32x2 a = {0.f, 0.f};
; #pragma unroll
;             for (int j = 0; j < 8; ++j) { const f32x4 w = *((const LAS f32x4*)(wr2 + e * DM) + F.lane + 64 * j);
; #pragma unroll
;                 for (int c = 0; c < 4; ++c) a += vv[j][c] * w[c]; }
;             lg[e] = a; }
	v_pk_fma_f32 v[178:179], v[68:69], v[224:225], v[178:179] op_sel_hi:[1,0,1]
	s_nop 0
	v_pk_fma_f32 v[174:175], v[70:71], v[224:225], v[178:179] op_sel:[0,1,0]
	s_nop 0
	v_pk_fma_f32 v[174:175], v[72:73], v[226:227], v[174:175] op_sel_hi:[1,0,1]
	v_mov_b32_e32 v176, v227
	v_pk_fma_f32 v[174:175], v[74:75], v[176:177], v[174:175] op_sel_hi:[1,0,1]
	ds_read_b128 v[240:243], v244 offset:35840
	s_waitcnt lgkmcnt(3)
	v_pk_fma_f32 v[180:181], v[124:125], v[228:229], 0 op_sel_hi:[1,0,0]
	s_nop 0
	v_pk_fma_f32 v[176:177], v[126:127], v[228:229], v[180:181] op_sel:[0,1,0]
	s_nop 0
	v_pk_fma_f32 v[176:177], v[128:129], v[230:231], v[176:177] op_sel_hi:[1,0,1]
	v_mov_b32_e32 v178, v231
	v_pk_fma_f32 v[180:181], v[130:131], v[178:179], v[176:177] op_sel_hi:[1,0,1]
	ds_read_b128 v[224:227], v244 offset:36864
	s_waitcnt lgkmcnt(3)
	v_pk_fma_f32 v[180:181], v[112:113], v[232:233], v[180:181] op_sel_hi:[1,0,1]
	s_nop 0
	v_pk_fma_f32 v[176:177], v[114:115], v[232:233], v[180:181] op_sel:[0,1,0]
	s_nop 0
	v_pk_fma_f32 v[176:177], v[118:119], v[234:235], v[176:177] op_sel_hi:[1,0,1]
	v_mov_b32_e32 v178, v235
	v_pk_fma_f32 v[180:181], v[122:123], v[178:179], v[176:177] op_sel_hi:[1,0,1]
	ds_read_b128 v[228:231], v244 offset:37888
	s_waitcnt lgkmcnt(3)
	v_pk_fma_f32 v[180:181], v[108:109], v[236:237], v[180:181] op_sel_hi:[1,0,1]
	s_nop 0
	v_pk_fma_f32 v[176:177], v[110:111], v[236:237], v[180:181] op_sel:[0,1,0]
	s_nop 0
	v_pk_fma_f32 v[176:177], v[116:117], v[238:239], v[176:177] op_sel_hi:[1,0,1]
	v_mov_b32_e32 v178, v239
	v_pk_fma_f32 v[180:181], v[120:121], v[178:179], v[176:177] op_sel_hi:[1,0,1]
	ds_read_b128 v[232:235], v244 offset:38912
	s_waitcnt lgkmcnt(3)
	v_pk_fma_f32 v[180:181], v[96:97], v[240:241], v[180:181] op_sel_hi:[1,0,1]
	s_nop 0
	v_pk_fma_f32 v[176:177], v[98:99], v[240:241], v[180:181] op_sel:[0,1,0]
	s_nop 0
	v_pk_fma_f32 v[176:177], v[102:103], v[242:243], v[176:177] op_sel_hi:[1,0,1]
	v_mov_b32_e32 v178, v243
	v_pk_fma_f32 v[180:181], v[106:107], v[178:179], v[176:177] op_sel_hi:[1,0,1]
	ds_read_b128 v[236:239], v244 offset:39936
	s_waitcnt lgkmcnt(3)
	v_pk_fma_f32 v[180:181], v[92:93], v[224:225], v[180:181] op_sel_hi:[1,0,1]
	s_nop 0
	v_pk_fma_f32 v[176:177], v[94:95], v[224:225], v[180:181] op_sel:[0,1,0]
	s_nop 0
	v_pk_fma_f32 v[176:177], v[100:101], v[226:227], v[176:177] op_sel_hi:[1,0,1]
	v_mov_b32_e32 v178, v227
	v_pk_fma_f32 v[180:181], v[104:105], v[178:179], v[176:177] op_sel_hi:[1,0,1]
	ds_read_b128 v[240:243], v244 offset:40960
	s_waitcnt lgkmcnt(3)
	v_pk_fma_f32 v[180:181], v[80:81], v[228:229], v[180:181] op_sel_hi:[1,0,1]
	s_nop 0
	v_pk_fma_f32 v[176:177], v[82:83], v[228:229], v[180:181] op_sel:[0,1,0]
	s_nop 0
	v_pk_fma_f32 v[176:177], v[86:87], v[230:231], v[176:177] op_sel_hi:[1,0,1]
	v_mov_b32_e32 v178, v231
	v_pk_fma_f32 v[180:181], v[90:91], v[178:179], v[176:177] op_sel_hi:[1,0,1]
	ds_read_b128 v[224:227], v244 offset:41984
	s_waitcnt lgkmcnt(3)
	v_pk_fma_f32 v[180:181], v[76:77], v[232:233], v[180:181] op_sel_hi:[1,0,1]
	s_nop 0
	v_pk_fma_f32 v[176:177], v[78:79], v[232:233], v[180:181] op_sel:[0,1,0]
	s_nop 0
	v_pk_fma_f32 v[176:177], v[84:85], v[234:235], v[176:177] op_sel_hi:[1,0,1]
	v_mov_b32_e32 v178, v235
	v_pk_fma_f32 v[180:181], v[88:89], v[178:179], v[176:177] op_sel_hi:[1,0,1]
	ds_read_b128 v[228:231], v244 offset:43008
	s_waitcnt lgkmcnt(3)
	v_pk_fma_f32 v[180:181], v[68:69], v[236:237], v[180:181] op_sel_hi:[1,0,1]
	s_nop 0
	v_pk_fma_f32 v[176:177], v[70:71], v[236:237], v[180:181] op_sel:[0,1,0]
	s_nop 0
	v_pk_fma_f32 v[176:177], v[72:73], v[238:239], v[176:177] op_sel_hi:[1,0,1]
	v_mov_b32_e32 v178, v239
	v_pk_fma_f32 v[176:177], v[74:75], v[178:179], v[176:177] op_sel_hi:[1,0,1]
	ds_read_b128 v[232:235], v244 offset:44032
	s_waitcnt lgkmcnt(3)
	v_pk_fma_f32 v[184:185], v[124:125], v[240:241], 0 op_sel_hi:[1,0,0]
	s_nop 0
	v_pk_fma_f32 v[178:179], v[126:127], v[240:241], v[184:185] op_sel:[0,1,0]
	s_nop 0
	v_pk_fma_f32 v[178:179], v[128:129], v[242:243], v[178:179] op_sel_hi:[1,0,1]
	v_mov_b32_e32 v180, v243
	v_pk_fma_f32 v[184:185], v[130:131], v[180:181], v[178:179] op_sel_hi:[1,0,1]
	ds_read_b128 v[236:239], v244 offset:45056
	s_waitcnt lgkmcnt(3)
	v_pk_fma_f32 v[184:185], v[112:113], v[224:225], v[184:185] op_sel_hi:[1,0,1]
	s_nop 0
	v_pk_fma_f32 v[178:179], v[114:115], v[224:225], v[184:185] op_sel:[0,1,0]
	s_nop 0
	v_pk_fma_f32 v[178:179], v[118:119], v[226:227], v[178:179] op_sel_hi:[1,0,1]
	v_mov_b32_e32 v180, v227
	v_pk_fma_f32 v[184:185], v[122:123], v[180:181], v[178:179] op_sel_hi:[1,0,1]
	ds_read_b128 v[240:243], v244 offset:46080
	s_waitcnt lgkmcnt(3)
	v_pk_fma_f32 v[184:185], v[108:109], v[228:229], v[184:185] op_sel_hi:[1,0,1]
	s_nop 0
	v_pk_fma_f32 v[178:179], v[110:111], v[228:229], v[184:185] op_sel:[0,1,0]
	s_nop 0
	v_pk_fma_f32 v[178:179], v[116:117], v[230:231], v[178:179] op_sel_hi:[1,0,1]
	v_mov_b32_e32 v180, v231
	v_pk_fma_f32 v[184:185], v[120:121], v[180:181], v[178:179] op_sel_hi:[1,0,1]
	ds_read_b128 v[224:227], v244 offset:47104
	s_waitcnt lgkmcnt(3)
	v_pk_fma_f32 v[184:185], v[96:97], v[232:233], v[184:185] op_sel_hi:[1,0,1]
	s_nop 0
	v_pk_fma_f32 v[178:179], v[98:99], v[232:233], v[184:185] op_sel:[0,1,0]
	s_nop 0
	v_pk_fma_f32 v[178:179], v[102:103], v[234:235], v[178:179] op_sel_hi:[1,0,1]
	v_mov_b32_e32 v180, v235
	v_pk_fma_f32 v[184:185], v[106:107], v[180:181], v[178:179] op_sel_hi:[1,0,1]
	ds_read_b128 v[228:231], v244 offset:48128
	s_waitcnt lgkmcnt(3)
; #define LAS __attribute__((address_space(3)))
; __device__ __forceinline__ void phase_norm2(const Params& p, const Ctx& F, const int l) {
;     ...
;         f32x2 lg[16];
;         unsigned wro = (unsigned)(uintptr_t)wr; asm volatile("" : "+v"(wro));
;         const LAS float* wr2 = (const LAS float*)(uintptr_t)wro;
; #pragma unroll
;         for (int e = 0; e < 16; ++e) { f32x2 a = {0.f, 0.f};
; #pragma unroll
;             for (int j = 0; j < 8; ++j) { const f32x4 w = *((const LAS f32x4*)(wr2 + e * DM) + F.lane + 64 * j);
; #pragma unroll
;                 for (int c = 0; c < 4; ++c) a += vv[j][c] * w[c]; }
;             lg[e] = a; }
	v_pk_fma_f32 v[184:185], v[92:93], v[236:237], v[184:185] op_sel_hi:[1,0,1]
	s_nop 0
	v_pk_fma_f32 v[178:179], v[94:95], v[236:237], v[184:185] op_sel:[0,1,0]
	s_nop 0
	v_pk_fma_f32 v[178:179], v[100:101], v[238:239], v[178:179] op_sel_hi:[1,0,1]
	v_mov_b32_e32 v180, v239
	v_pk_fma_f32 v[184:185], v[104:105], v[180:181], v[178:179] op_sel_hi:[1,0,1]
	ds_read_b128 v[232:235], v244 offset:49152
	s_waitcnt lgkmcnt(3)
	v_pk_fma_f32 v[184:185], v[80:81], v[240:241], v[184:185] op_sel_hi:[1,0,1]
	s_nop 0
	v_pk_fma_f32 v[178:179], v[82:83], v[240:241], v[184:185] op_sel:[0,1,0]
	s_nop 0
	v_pk_fma_f32 v[178:179], v[86:87], v[242:243], v[178:179] op_sel_hi:[1,0,1]
	v_mov_b32_e32 v180, v243
	v_pk_fma_f32 v[184:185], v[90:91], v[180:181], v[178:179] op_sel_hi:[1,0,1]
	ds_read_b128 v[236:239], v244 offset:50176
	s_waitcnt lgkmcnt(3)
	v_pk_fma_f32 v[184:185], v[76:77], v[224:225], v[184:185] op_sel_hi:[1,0,1]
	s_nop 0
	v_pk_fma_f32 v[178:179], v[78:79], v[224:225], v[184:185] op_sel:[0,1,0]
	s_nop 0
	v_pk_fma_f32 v[178:179], v[84:85], v[226:227], v[178:179] op_sel_hi:[1,0,1]
	v_mov_b32_e32 v180, v227
	v_pk_fma_f32 v[184:185], v[88:89], v[180:181], v[178:179] op_sel_hi:[1,0,1]
	ds_read_b128 v[240:243], v244 offset:51200
	s_waitcnt lgkmcnt(3)
	v_pk_fma_f32 v[184:185], v[68:69], v[228:229], v[184:185] op_sel_hi:[1,0,1]
	s_nop 0
	v_pk_fma_f32 v[178:179], v[70:71], v[228:229], v[184:185] op_sel:[0,1,0]
	ds_read_b128 v[224:227], v244 offset:52224
	v_pk_fma_f32 v[178:179], v[72:73], v[230:231], v[178:179] op_sel_hi:[1,0,1]
	v_mov_b32_e32 v180, v231
	v_pk_fma_f32 v[178:179], v[74:75], v[180:181], v[178:179] op_sel_hi:[1,0,1]
	s_waitcnt lgkmcnt(3)
	v_pk_fma_f32 v[180:181], v[124:125], v[232:233], 0 op_sel_hi:[1,0,0]
	s_nop 0
	v_pk_fma_f32 v[180:181], v[126:127], v[232:233], v[180:181] op_sel:[0,1,0]
	v_mov_b32_e32 v184, v235
	v_pk_fma_f32 v[180:181], v[128:129], v[234:235], v[180:181] op_sel_hi:[1,0,1]
	s_nop 0
	v_pk_fma_f32 v[180:181], v[130:131], v[184:185], v[180:181] op_sel_hi:[1,0,1]
	ds_read_b128 v[228:231], v244 offset:53248
	s_waitcnt lgkmcnt(3)
	v_pk_fma_f32 v[180:181], v[112:113], v[236:237], v[180:181] op_sel_hi:[1,0,1]
	s_nop 0
	v_pk_fma_f32 v[180:181], v[114:115], v[236:237], v[180:181] op_sel:[0,1,0]
	v_mov_b32_e32 v184, v239
	v_pk_fma_f32 v[180:181], v[118:119], v[238:239], v[180:181] op_sel_hi:[1,0,1]
	s_nop 0
	v_pk_fma_f32 v[180:181], v[122:123], v[184:185], v[180:181] op_sel_hi:[1,0,1]
	ds_read_b128 v[232:235], v244 offset:54272
	s_waitcnt lgkmcnt(3)
	v_pk_fma_f32 v[180:181], v[108:109], v[240:241], v[180:181] op_sel_hi:[1,0,1]
	s_nop 0
	v_pk_fma_f32 v[180:181], v[110:111], v[240:241], v[180:181] op_sel:[0,1,0]
	v_mov_b32_e32 v184, v243
	v_pk_fma_f32 v[180:181], v[116:117], v[242:243], v[180:181] op_sel_hi:[1,0,1]
	s_nop 0
	v_pk_fma_f32 v[180:181], v[120:121], v[184:185], v[180:181] op_sel_hi:[1,0,1]
	ds_read_b128 v[236:239], v244 offset:55296
	s_waitcnt lgkmcnt(3)
	v_pk_fma_f32 v[180:181], v[96:97], v[224:225], v[180:181] op_sel_hi:[1,0,1]
	s_nop 0
	v_pk_fma_f32 v[180:181], v[98:99], v[224:225], v[180:181] op_sel:[0,1,0]
	v_mov_b32_e32 v184, v227
	v_pk_fma_f32 v[180:181], v[102:103], v[226:227], v[180:181] op_sel_hi:[1,0,1]
	s_nop 0
	v_pk_fma_f32 v[180:181], v[106:107], v[184:185], v[180:181] op_sel_hi:[1,0,1]
	ds_read_b128 v[240:243], v244 offset:56320
	s_waitcnt lgkmcnt(3)
	v_pk_fma_f32 v[180:181], v[92:93], v[228:229], v[180:181] op_sel_hi:[1,0,1]
	s_nop 0
	v_pk_fma_f32 v[180:181], v[94:95], v[228:229], v[180:181] op_sel:[0,1,0]
	v_mov_b32_e32 v184, v231
	v_pk_fma_f32 v[180:181], v[100:101], v[230:231], v[180:181] op_sel_hi:[1,0,1]
	s_nop 0
	v_pk_fma_f32 v[180:181], v[104:105], v[184:185], v[180:181] op_sel_hi:[1,0,1]
	ds_read_b128 v[224:227], v244 offset:57344
	s_waitcnt lgkmcnt(3)
	v_pk_fma_f32 v[180:181], v[80:81], v[232:233], v[180:181] op_sel_hi:[1,0,1]
	s_nop 0
	v_pk_fma_f32 v[180:181], v[82:83], v[232:233], v[180:181] op_sel:[0,1,0]
	v_mov_b32_e32 v184, v235
	v_pk_fma_f32 v[180:181], v[86:87], v[234:235], v[180:181] op_sel_hi:[1,0,1]
	s_nop 0
	v_pk_fma_f32 v[180:181], v[90:91], v[184:185], v[180:181] op_sel_hi:[1,0,1]
	ds_read_b128 v[228:231], v244 offset:58368
	s_waitcnt lgkmcnt(3)
	v_pk_fma_f32 v[180:181], v[76:77], v[236:237], v[180:181] op_sel_hi:[1,0,1]
	s_nop 0
	v_pk_fma_f32 v[180:181], v[78:79], v[236:237], v[180:181] op_sel:[0,1,0]
	v_mov_b32_e32 v184, v239
	v_pk_fma_f32 v[180:181], v[84:85], v[238:239], v[180:181] op_sel_hi:[1,0,1]
	s_nop 0
	v_pk_fma_f32 v[180:181], v[88:89], v[184:185], v[180:181] op_sel_hi:[1,0,1]
	ds_read_b128 v[232:235], v244 offset:59392
	s_waitcnt lgkmcnt(3)
	v_pk_fma_f32 v[180:181], v[68:69], v[240:241], v[180:181] op_sel_hi:[1,0,1]
	s_nop 0
	v_pk_fma_f32 v[180:181], v[70:71], v[240:241], v[180:181] op_sel:[0,1,0]
	v_mov_b32_e32 v184, v243
	v_pk_fma_f32 v[180:181], v[72:73], v[242:243], v[180:181] op_sel_hi:[1,0,1]
	s_nop 0
	v_pk_fma_f32 v[180:181], v[74:75], v[184:185], v[180:181] op_sel_hi:[1,0,1]
	ds_read_b128 v[236:239], v244 offset:60416
	s_waitcnt lgkmcnt(3)
	v_pk_fma_f32 v[124:125], v[124:125], v[224:225], 0 op_sel_hi:[1,0,0]
	s_nop 0
	v_pk_fma_f32 v[124:125], v[126:127], v[224:225], v[124:125] op_sel:[0,1,0]
	v_mov_b32_e32 v126, v227
	v_pk_fma_f32 v[124:125], v[128:129], v[226:227], v[124:125] op_sel_hi:[1,0,1]
	s_nop 0
	v_pk_fma_f32 v[128:129], v[130:131], v[126:127], v[124:125] op_sel_hi:[1,0,1]
	ds_read_b128 v[240:243], v244 offset:61440
	s_waitcnt lgkmcnt(3)
	v_pk_fma_f32 v[112:113], v[112:113], v[228:229], v[128:129] op_sel_hi:[1,0,1]
	s_nop 0
	v_pk_fma_f32 v[112:113], v[114:115], v[228:229], v[112:113] op_sel:[0,1,0]
	v_mov_b32_e32 v114, v231
	v_pk_fma_f32 v[112:113], v[118:119], v[230:231], v[112:113] op_sel_hi:[1,0,1]
	s_nop 0
	v_pk_fma_f32 v[118:119], v[122:123], v[114:115], v[112:113] op_sel_hi:[1,0,1]
	ds_read_b128 v[224:227], v244 offset:62464
	s_waitcnt lgkmcnt(3)
; #define LAS __attribute__((address_space(3)))
; __device__ __forceinline__ void router_tail(const Ctx& F, const float (&lg)[16], const int b, const int t, const bool valid) {
;     const bool b5 = (F.lane & 32) != 0, b4 = (F.lane & 16) != 0, b3 = (F.lane & 8) != 0, b2 = (F.lane & 4) != 0;
;     float r8[8], r4[4], r2[2];
; #pragma unroll
;     for (int e = 0; e < 8; ++e) { const float keep = b5 ? lg[e + 8] : lg[e], send = b5 ? lg[e] : lg[e + 8]; r8[e] = keep + __shfl_xor(send, 32); }
; #pragma unroll
;     for (int e = 0; e < 4; ++e) { const float keep = b4 ? r8[e + 4] : r8[e], send = b4 ? r8[e] : r8[e + 4]; r4[e] = keep + __shfl_xor(send, 16); }
; #pragma unroll
;     for (int e = 0; e < 2; ++e) { const float keep = b3 ? r4[e + 2] : r4[e], send = b3 ? r4[e] : r4[e + 2]; r2[e] = keep + __shfl_xor(send, 8); }
;     float lgt; { const float keep = b2 ? r2[1] : r2[0], send = b2 ? r2[0] : r2[1]; lgt = keep + __shfl_xor(send, 4); }
;     lgt += __shfl_xor(lgt, 2); lgt += __shfl_xor(lgt, 1);
;     float mx = lgt;
;     mx = fmaxf(mx, __shfl_xor(mx, 4)); mx = fmaxf(mx, __shfl_xor(mx, 8)); mx = fmaxf(mx, __shfl_xor(mx, 16)); mx = fmaxf(mx, __shfl_xor(mx, 32));
;     const float ex = expf(lgt - mx); float sum = ex;
;     sum += __shfl_xor(sum, 4); sum += __shfl_xor(sum, 8); sum += __shfl_xor(sum, 16); sum += __shfl_xor(sum, 32);
;     if (valid && (F.lane & 3) == 0) { const float af = ex / sum; const int e = F.lane >> 2;
;         if (t < CTXL) F.affc[((size_t)(b * 16 + e)) * CTXL + t] = af; else F.affl[((size_t)(b * 16 + e)) * SEQ + (t - CTXL)] = af; }
; __device__ __forceinline__ void phase_norm2(const Params& p, const Ctx& F, const int l) {
;     ...
;         for (int e = 0; e < 16; ++e) { f32x2 a = {0.f, 0.f};
; #pragma unroll
;             for (int j = 0; j < 8; ++j) { const f32x4 w = *((const LAS f32x4*)(wr2 + e * DM) + F.lane + 64 * j);
; #pragma unroll
;                 for (int c = 0; c < 4; ++c) a += vv[j][c] * w[c]; }
;             lg[e] = a; }
	v_pk_fma_f32 v[108:109], v[108:109], v[232:233], v[118:119] op_sel_hi:[1,0,1]
	s_nop 0
	v_pk_fma_f32 v[108:109], v[110:111], v[232:233], v[108:109] op_sel:[0,1,0]
	v_mov_b32_e32 v110, v235
	v_pk_fma_f32 v[108:109], v[116:117], v[234:235], v[108:109] op_sel_hi:[1,0,1]
	s_nop 0
	v_pk_fma_f32 v[112:113], v[120:121], v[110:111], v[108:109] op_sel_hi:[1,0,1]
	ds_read_b128 v[228:231], v244 offset:63488
	s_waitcnt lgkmcnt(3)
	v_pk_fma_f32 v[96:97], v[96:97], v[236:237], v[112:113] op_sel_hi:[1,0,1]
	s_nop 0
	v_pk_fma_f32 v[96:97], v[98:99], v[236:237], v[96:97] op_sel:[0,1,0]
	v_mov_b32_e32 v98, v239
	v_pk_fma_f32 v[96:97], v[102:103], v[238:239], v[96:97] op_sel_hi:[1,0,1]
	s_nop 0
	v_pk_fma_f32 v[102:103], v[106:107], v[98:99], v[96:97] op_sel_hi:[1,0,1]
	ds_read_b128 v[232:235], v244 offset:64512
	s_waitcnt lgkmcnt(3)
	v_pk_fma_f32 v[92:93], v[92:93], v[240:241], v[102:103] op_sel_hi:[1,0,1]
	s_nop 0
	v_pk_fma_f32 v[92:93], v[94:95], v[240:241], v[92:93] op_sel:[0,1,0]
	v_mov_b32_e32 v94, v243
	v_pk_fma_f32 v[92:93], v[100:101], v[242:243], v[92:93] op_sel_hi:[1,0,1]
	s_nop 0
	v_pk_fma_f32 v[96:97], v[104:105], v[94:95], v[92:93] op_sel_hi:[1,0,1]
	s_waitcnt lgkmcnt(2)
	v_pk_fma_f32 v[80:81], v[80:81], v[224:225], v[96:97] op_sel_hi:[1,0,1]
	s_nop 0
	v_pk_fma_f32 v[80:81], v[82:83], v[224:225], v[80:81] op_sel:[0,1,0]
	v_mov_b32_e32 v82, v227
	v_pk_fma_f32 v[80:81], v[86:87], v[226:227], v[80:81] op_sel_hi:[1,0,1]
	s_nop 0
	v_pk_fma_f32 v[86:87], v[90:91], v[82:83], v[80:81] op_sel_hi:[1,0,1]
	s_waitcnt lgkmcnt(1)
	v_pk_fma_f32 v[76:77], v[76:77], v[228:229], v[86:87] op_sel_hi:[1,0,1]
	s_nop 0
	v_pk_fma_f32 v[76:77], v[78:79], v[228:229], v[76:77] op_sel:[0,1,0]
	v_mov_b32_e32 v78, v231
	v_pk_fma_f32 v[76:77], v[84:85], v[230:231], v[76:77] op_sel_hi:[1,0,1]
	s_nop 0
	v_pk_fma_f32 v[80:81], v[88:89], v[78:79], v[76:77] op_sel_hi:[1,0,1]
	v_cndmask_b32_e64 v1, v168, v152, s[38:39]
	s_waitcnt lgkmcnt(0)
	v_pk_fma_f32 v[68:69], v[68:69], v[232:233], v[80:81] op_sel_hi:[1,0,1]
	s_nop 0
	v_pk_fma_f32 v[68:69], v[70:71], v[232:233], v[68:69] op_sel:[0,1,0]
	v_mov_b32_e32 v70, v235
	v_pk_fma_f32 v[68:69], v[72:73], v[234:235], v[68:69] op_sel_hi:[1,0,1]
	v_cndmask_b32_e64 v72, v156, v172, s[38:39]
	v_pk_fma_f32 v[68:69], v[74:75], v[70:71], v[68:69] op_sel_hi:[1,0,1]
	s_nop 1
	v_permlane32_swap_b32_e32 v152, v168
	v_permlane32_swap_b32_e32 v154, v170
	v_permlane32_swap_b32_e32 v156, v172
	v_permlane32_swap_b32_e32 v158, v174
	v_permlane32_swap_b32_e32 v160, v176
	v_permlane32_swap_b32_e32 v162, v178
	v_permlane32_swap_b32_e32 v164, v180
	v_permlane32_swap_b32_e32 v166, v68
	v_add_f32_e32 v1, v152, v168
	v_add_f32_e32 v70, v154, v170
	v_add_f32_e32 v71, v156, v172
	v_add_f32_e32 v72, v158, v174
	v_add_f32_e32 v73, v160, v176
	v_add_f32_e32 v74, v162, v178
	v_add_f32_e32 v75, v164, v180
	v_add_f32_e32 v68, v166, v68
	s_waitcnt lgkmcnt(0)
	v_cndmask_b32_e64 v76, v73, v1, s[40:41]
	v_cndmask_b32_e64 v1, v1, v73, s[40:41]
	v_cndmask_b32_e64 v73, v74, v70, s[40:41]
	v_cndmask_b32_e64 v70, v70, v74, s[40:41]
	ds_bpermute_b32 v70, v193, v70
	ds_bpermute_b32 v1, v193, v1
	s_waitcnt lgkmcnt(1)
	v_add_f32_e32 v70, v73, v70
	v_cndmask_b32_e64 v73, v75, v71, s[40:41]
	v_cndmask_b32_e64 v71, v71, v75, s[40:41]
	ds_bpermute_b32 v71, v193, v71
	s_waitcnt lgkmcnt(1)
	v_add_f32_e32 v1, v76, v1
	s_waitcnt lgkmcnt(0)
	v_add_f32_e32 v71, v73, v71
	v_cndmask_b32_e64 v73, v68, v72, s[40:41]
	v_cndmask_b32_e64 v68, v72, v68, s[40:41]
	ds_bpermute_b32 v68, v193, v68
	v_cndmask_b32_e64 v72, v71, v1, s[42:43]
	v_cndmask_b32_e64 v1, v1, v71, s[42:43]
	ds_bpermute_b32 v1, v192, v1
	s_waitcnt lgkmcnt(1)
	v_add_f32_e32 v68, v73, v68
	v_cndmask_b32_e64 v71, v68, v70, s[42:43]
	v_cndmask_b32_e64 v68, v70, v68, s[42:43]
	ds_bpermute_b32 v68, v192, v68
	s_waitcnt lgkmcnt(1)
	v_add_f32_e32 v1, v72, v1
	s_waitcnt lgkmcnt(0)
	v_add_f32_e32 v68, v71, v68
	v_cndmask_b32_e64 v70, v68, v1, s[4:5]
	v_cndmask_b32_e64 v1, v1, v68, s[4:5]
	ds_bpermute_b32 v1, v191, v1
	s_waitcnt lgkmcnt(0)
	v_add_f32_e32 v1, v70, v1
	ds_bpermute_b32 v68, v190, v1
	s_waitcnt lgkmcnt(0)
	v_add_f32_e32 v1, v1, v68
	ds_bpermute_b32 v68, v133, v1
	s_waitcnt lgkmcnt(0)
	v_add_f32_e32 v1, v1, v68
	ds_bpermute_b32 v68, v191, v1
	s_waitcnt lgkmcnt(0)
	v_max_f32_e32 v68, v68, v68
	v_max_f32_e32 v68, v1, v68
	ds_bpermute_b32 v70, v192, v68
	s_waitcnt lgkmcnt(0)
	v_max_f32_e32 v70, v70, v70
	v_max_f32_e32 v68, v68, v70
	ds_bpermute_b32 v70, v193, v68
	s_waitcnt lgkmcnt(0)
	v_max_f32_e32 v70, v70, v70
	v_max_f32_e32 v68, v68, v70
	ds_bpermute_b32 v70, v194, v68
	s_waitcnt lgkmcnt(0)
	v_max_f32_e32 v70, v70, v70
	v_max_f32_e32 v68, v68, v70
	v_sub_f32_e32 v1, v1, v68
	v_mul_f32_e32 v68, 0x3fb8aa3b, v1
	v_fma_f32 v70, v1, s55, -v68
	v_rndne_f32_e32 v71, v68
	v_fmac_f32_e32 v70, 0x32a5705f, v1
	v_sub_f32_e32 v68, v68, v71
	v_add_f32_e32 v68, v68, v70
	v_exp_f32_e32 v68, v68
	v_cvt_i32_f32_e32 v70, v71
	v_cmp_ngt_f32_e32 vcc, s56, v1
	v_ldexp_f32 v68, v68, v70
	s_nop 0
	v_cndmask_b32_e32 v68, 0, v68, vcc
	v_cmp_nlt_f32_e32 vcc, s57, v1
	s_nop 1
	v_cndmask_b32_e32 v68, v222, v68, vcc
	ds_bpermute_b32 v1, v191, v68
	s_waitcnt lgkmcnt(0)
	v_add_f32_e32 v1, v68, v1
	ds_bpermute_b32 v70, v192, v1
	s_waitcnt lgkmcnt(0)
	v_add_f32_e32 v1, v1, v70
	ds_bpermute_b32 v70, v193, v1
	s_waitcnt lgkmcnt(0)
	v_add_f32_e32 v70, v1, v70
	ds_bpermute_b32 v71, v194, v70
	s_and_saveexec_b64 s[0:1], s[6:7]
	s_cbranch_execz .LBB0_942
	s_waitcnt lgkmcnt(0)
	v_add_f32_e32 v1, v70, v71
	v_div_scale_f32 v70, s[12:13], v1, v1, v68
	v_rcp_f32_e32 v71, v70
	v_div_scale_f32 v72, vcc, v68, v1, v68
	s_cmpk_gt_i32 s60, 0xff
	v_fma_f32 v73, -v70, v71, 1.0
	v_fmac_f32_e32 v71, v73, v71
	v_mul_f32_e32 v73, v72, v71
	v_fma_f32 v74, -v70, v73, v72
	v_fmac_f32_e32 v73, v74, v71
	v_fma_f32 v70, -v70, v73, v72
	v_div_fmas_f32 v70, v70, v71, v73
	v_div_fixup_f32 v68, v70, v1, v68
	s_mov_b64 s[12:13], -1
	s_cbranch_scc0 .LBB0_940
	v_lshl_add_u64 v[70:71], s[60:61], 2, v[148:149]
	global_store_dword v[70:71], v68, off offset:-1024
	s_mov_b64 s[12:13], 0

; __device__ __forceinline__ void router_tail(const Ctx& F, const float (&lg)[16], const int b, const int t, const bool valid) {
;     const bool b5 = (F.lane & 32) != 0, b4 = (F.lane & 16) != 0, b3 = (F.lane & 8) != 0, b2 = (F.lane & 4) != 0;
;     float r8[8], r4[4], r2[2];
; #pragma unroll
;     for (int e = 0; e < 8; ++e) { const float keep = b5 ? lg[e + 8] : lg[e], send = b5 ? lg[e] : lg[e + 8]; r8[e] = keep + __shfl_xor(send, 32); }
; #pragma unroll
;     for (int e = 0; e < 4; ++e) { const float keep = b4 ? r8[e + 4] : r8[e], send = b4 ? r8[e] : r8[e + 4]; r4[e] = keep + __shfl_xor(send, 16); }
; #pragma unroll
;     for (int e = 0; e < 2; ++e) { const float keep = b3 ? r4[e + 2] : r4[e], send = b3 ? r4[e] : r4[e + 2]; r2[e] = keep + __shfl_xor(send, 8); }
;     float lgt; { const float keep = b2 ? r2[1] : r2[0], send = b2 ? r2[0] : r2[1]; lgt = keep + __shfl_xor(send, 4); }
;     lgt += __shfl_xor(lgt, 2); lgt += __shfl_xor(lgt, 1);
;     float mx = lgt;
;     mx = fmaxf(mx, __shfl_xor(mx, 4)); mx = fmaxf(mx, __shfl_xor(mx, 8)); mx = fmaxf(mx, __shfl_xor(mx, 16)); mx = fmaxf(mx, __shfl_xor(mx, 32));
;     const float ex = expf(lgt - mx); float sum = ex;
;     sum += __shfl_xor(sum, 4); sum += __shfl_xor(sum, 8); sum += __shfl_xor(sum, 16); sum += __shfl_xor(sum, 32);
;     if (valid && (F.lane & 3) == 0) { const float af = ex / sum; const int e = F.lane >> 2;
;         if (t < CTXL) F.affc[((size_t)(b * 16 + e)) * CTXL + t] = af; else F.affl[((size_t)(b * 16 + e)) * SEQ + (t - CTXL)] = af; }
; }
.LBB0_942:
	s_or_b64 exec, exec, s[0:1]
	s_and_b64 s[8:9], s[6:7], s[8:9]
	s_waitcnt lgkmcnt(0)
	s_nop 1
	v_permlane32_swap_b32_e32 v153, v169
	v_permlane32_swap_b32_e32 v155, v171
	v_permlane32_swap_b32_e32 v157, v173
	v_permlane32_swap_b32_e32 v159, v175
	v_permlane32_swap_b32_e32 v161, v177
	v_permlane32_swap_b32_e32 v163, v179
	v_permlane32_swap_b32_e32 v165, v181
	v_permlane32_swap_b32_e32 v167, v69
	v_add_f32_e32 v1, v153, v169
	v_add_f32_e32 v68, v155, v171
	v_add_f32_e32 v70, v157, v173
	v_add_f32_e32 v71, v159, v175
	v_add_f32_e32 v72, v161, v177
	v_add_f32_e32 v73, v163, v179
	v_add_f32_e32 v74, v165, v181
	v_add_f32_e32 v69, v167, v69
	s_waitcnt lgkmcnt(0)
	v_cndmask_b32_e64 v75, v72, v1, s[40:41]
	v_cndmask_b32_e64 v1, v1, v72, s[40:41]
	v_cndmask_b32_e64 v72, v73, v68, s[40:41]
	v_cndmask_b32_e64 v68, v68, v73, s[40:41]
	ds_bpermute_b32 v68, v193, v68
	ds_bpermute_b32 v1, v193, v1
	s_waitcnt lgkmcnt(1)
	v_add_f32_e32 v68, v72, v68
	v_cndmask_b32_e64 v72, v74, v70, s[40:41]
	v_cndmask_b32_e64 v70, v70, v74, s[40:41]
	ds_bpermute_b32 v70, v193, v70
	s_waitcnt lgkmcnt(1)
	v_add_f32_e32 v1, v75, v1
	s_waitcnt lgkmcnt(0)
	v_add_f32_e32 v70, v72, v70
	v_cndmask_b32_e64 v72, v69, v71, s[40:41]
	v_cndmask_b32_e64 v69, v71, v69, s[40:41]
	ds_bpermute_b32 v69, v193, v69
	v_cndmask_b32_e64 v71, v70, v1, s[42:43]
	v_cndmask_b32_e64 v1, v1, v70, s[42:43]
	ds_bpermute_b32 v1, v192, v1
	s_waitcnt lgkmcnt(1)
	v_add_f32_e32 v69, v72, v69
	v_cndmask_b32_e64 v70, v69, v68, s[42:43]
	v_cndmask_b32_e64 v68, v68, v69, s[42:43]
	ds_bpermute_b32 v68, v192, v68
	s_waitcnt lgkmcnt(1)
	v_add_f32_e32 v1, v71, v1
	s_waitcnt lgkmcnt(0)
	v_add_f32_e32 v68, v70, v68
	v_cndmask_b32_e64 v69, v68, v1, s[4:5]
	v_cndmask_b32_e64 v1, v1, v68, s[4:5]
	ds_bpermute_b32 v1, v191, v1
	s_waitcnt lgkmcnt(0)
	v_add_f32_e32 v1, v69, v1
	ds_bpermute_b32 v68, v190, v1
	s_waitcnt lgkmcnt(0)
	v_add_f32_e32 v1, v1, v68
	ds_bpermute_b32 v68, v133, v1
	s_waitcnt lgkmcnt(0)
	v_add_f32_e32 v1, v1, v68
	ds_bpermute_b32 v68, v191, v1
	s_waitcnt lgkmcnt(0)
	v_max_f32_e32 v68, v68, v68
	v_max_f32_e32 v68, v1, v68
	ds_bpermute_b32 v69, v192, v68
	s_waitcnt lgkmcnt(0)
	v_max_f32_e32 v69, v69, v69
	v_max_f32_e32 v68, v68, v69
	ds_bpermute_b32 v69, v193, v68
	s_waitcnt lgkmcnt(0)
	v_max_f32_e32 v69, v69, v69
	v_max_f32_e32 v68, v68, v69
	ds_bpermute_b32 v69, v194, v68
	s_waitcnt lgkmcnt(0)
	v_max_f32_e32 v69, v69, v69
	v_max_f32_e32 v68, v68, v69
	v_sub_f32_e32 v1, v1, v68
	v_mul_f32_e32 v68, 0x3fb8aa3b, v1
	v_fma_f32 v69, v1, s55, -v68
	v_rndne_f32_e32 v70, v68
	v_fmac_f32_e32 v69, 0x32a5705f, v1
	v_sub_f32_e32 v68, v68, v70
	v_add_f32_e32 v68, v68, v69
	v_exp_f32_e32 v68, v68
	v_cvt_i32_f32_e32 v69, v70
	v_cmp_ngt_f32_e32 vcc, s56, v1
	v_ldexp_f32 v68, v68, v69
	s_nop 0
	v_cndmask_b32_e32 v68, 0, v68, vcc
	v_cmp_nlt_f32_e32 vcc, s57, v1
	s_nop 1
	v_cndmask_b32_e32 v68, v222, v68, vcc
	ds_bpermute_b32 v1, v191, v68
	s_waitcnt lgkmcnt(0)
	v_add_f32_e32 v1, v68, v1
	ds_bpermute_b32 v69, v192, v1
	s_waitcnt lgkmcnt(0)
	v_add_f32_e32 v1, v1, v69
	ds_bpermute_b32 v69, v193, v1
	s_waitcnt lgkmcnt(0)
	v_add_f32_e32 v69, v1, v69
	ds_bpermute_b32 v70, v194, v69
	s_and_saveexec_b64 s[0:1], s[8:9]
	s_cbranch_execz .LBB0_911
	s_waitcnt lgkmcnt(0)
	v_add_f32_e32 v1, v69, v70
	v_div_scale_f32 v69, s[8:9], v1, v1, v68
	v_rcp_f32_e32 v70, v69
	v_div_scale_f32 v71, vcc, v68, v1, v68
	s_cmpk_gt_i32 s2, 0xff
	v_fma_f32 v72, -v69, v70, 1.0
	v_fmac_f32_e32 v70, v72, v70
	v_mul_f32_e32 v72, v71, v70
	v_fma_f32 v73, -v69, v72, v71
	v_fmac_f32_e32 v72, v73, v70
	v_fma_f32 v69, -v69, v72, v71
	v_div_fmas_f32 v69, v69, v70, v72
	v_div_fixup_f32 v68, v69, v1, v68
	s_mov_b64 s[8:9], -1
	s_cbranch_scc0 .LBB0_945
	s_mov_b32 s3, s61
	v_lshl_add_u64 v[70:71], s[2:3], 2, v[148:149]
	global_store_dword v[70:71], v68, off offset:-1024
	s_mov_b64 s[8:9], 0
